# v16
# baseline (speedup 1.0000x reference)
.Lnerf_hid_b_first:
	s_waitcnt vmcnt(0) lgkmcnt(0)
	s_barrier
	ds_read_b128 v[224:227], v121 offset:40960
	ds_read_b128 v[228:231], v121 offset:41984
	ds_read_b128 v[152:155], v183 offset:0
	ds_read_b128 v[156:159], v183 offset:64
	v_mfma_f32_16x16x32_bf16 v[80:83], v[240:243], v[208:211], 0
	ds_read_b128 v[232:235], v121 offset:43008
	v_cvt_pk_bf16_f32 v48, v64, v65
	v_cvt_pk_bf16_f32 v49, v66, v67
	v_mfma_f32_16x16x32_bf16 v[84:87], v[240:243], v[212:215], 0
	ds_read_b128 v[236:239], v121 offset:44032
	v_cvt_pk_bf16_f32 v52, v56, v57
	v_cvt_pk_bf16_f32 v53, v58, v59
	ds_read_b128 v[240:243], v121 offset:45056
	v_mfma_f32_16x16x32_bf16 v[76:79], v[244:247], v[208:211], 0
	v_cvt_pk_bf16_f32 v50, v68, v69
	v_cvt_pk_bf16_f32 v51, v70, v71
	v_mfma_f32_16x16x32_bf16 v[72:75], v[244:247], v[212:215], 0
	v_cvt_pk_bf16_f32 v54, v60, v61
	v_cvt_pk_bf16_f32 v55, v62, v63
	ds_read_b128 v[244:247], v121 offset:46080
	v_mfma_f32_16x16x32_bf16 v[80:83], v[248:251], v[216:219], v[80:83]
	v_pk_max_i16 v48, v48, 0
	v_pk_max_i16 v49, v49, 0
	v_mfma_f32_16x16x32_bf16 v[84:87], v[248:251], v[220:223], v[84:87]
	v_pk_max_i16 v50, v50, 0
	v_pk_max_i16 v51, v51, 0
	ds_read_b128 v[248:251], v121 offset:47104
	v_mfma_f32_16x16x32_bf16 v[76:79], v[252:255], v[216:219], v[76:79]
	v_pk_max_i16 v52, v52, 0
	v_pk_max_i16 v53, v53, 0
	v_mfma_f32_16x16x32_bf16 v[72:75], v[252:255], v[220:223], v[72:75]
	v_pk_max_i16 v54, v54, 0
	v_pk_max_i16 v55, v55, 0
	ds_read_b128 v[252:255], v121 offset:48128
	s_setprio 3
	s_waitcnt lgkmcnt(6)
	v_mfma_f32_16x16x32_bf16 v[64:67], v[224:227], v[0:3], v[152:155]
	v_mfma_f32_16x16x32_bf16 v[68:71], v[228:231], v[0:3], v[156:159]
	v_mfma_f32_16x16x32_bf16 v[60:63], v[228:231], v[4:7], v[156:159]
	v_mfma_f32_16x16x32_bf16 v[56:59], v[224:227], v[4:7], v[152:155]
	ds_read_b128 v[224:227], v121 offset:49152
	ds_read_b128 v[228:231], v121 offset:50176
	s_waitcnt lgkmcnt(6)
	ds_read_b128 v[160:163], v183 offset:128
	ds_read_b128 v[164:167], v183 offset:192
	v_mfma_f32_16x16x32_bf16 v[64:67], v[232:235], v[12:15], v[64:67]
	v_cvt_pk_bf16_f32 v112, v80, v81
	v_mfma_f32_16x16x32_bf16 v[68:71], v[236:239], v[12:15], v[68:71]
	v_cvt_pk_bf16_f32 v113, v82, v83
	v_mfma_f32_16x16x32_bf16 v[60:63], v[236:239], v[8:11], v[60:63]
	v_cvt_pk_bf16_f32 v114, v76, v77
	v_mfma_f32_16x16x32_bf16 v[56:59], v[232:235], v[8:11], v[56:59]
	v_cvt_pk_bf16_f32 v115, v78, v79
	ds_read_b128 v[232:235], v121 offset:51200
	ds_read_b128 v[236:239], v121 offset:52224
	s_waitcnt lgkmcnt(8)
	v_mfma_f32_16x16x32_bf16 v[64:67], v[240:243], v[16:19], v[64:67]
	v_cvt_pk_bf16_f32 v116, v84, v85
	v_mfma_f32_16x16x32_bf16 v[68:71], v[244:247], v[16:19], v[68:71]
	v_cvt_pk_bf16_f32 v117, v86, v87
	v_mfma_f32_16x16x32_bf16 v[60:63], v[244:247], v[20:23], v[60:63]
	v_cvt_pk_bf16_f32 v118, v72, v73
	v_mfma_f32_16x16x32_bf16 v[56:59], v[240:243], v[20:23], v[56:59]
	v_cvt_pk_bf16_f32 v119, v74, v75
	ds_read_b128 v[240:243], v121 offset:53248
	ds_read_b128 v[244:247], v121 offset:54272
	s_waitcnt lgkmcnt(8)
	v_mfma_f32_16x16x32_bf16 v[64:67], v[248:251], v[24:27], v[64:67]
	v_pk_max_i16 v112, v112, 0
	v_mfma_f32_16x16x32_bf16 v[68:71], v[252:255], v[24:27], v[68:71]
	v_pk_max_i16 v113, v113, 0
	v_mfma_f32_16x16x32_bf16 v[60:63], v[252:255], v[28:31], v[60:63]
	v_pk_max_i16 v114, v114, 0
	v_mfma_f32_16x16x32_bf16 v[56:59], v[248:251], v[28:31], v[56:59]
	v_pk_max_i16 v115, v115, 0
	ds_read_b128 v[248:251], v121 offset:55296
	ds_read_b128 v[252:255], v121 offset:56320
	s_setprio 2
	s_waitcnt lgkmcnt(8)
	v_mfma_f32_16x16x32_bf16 v[64:67], v[224:227], v[32:35], v[64:67]
	v_pk_max_i16 v116, v116, 0
	v_mfma_f32_16x16x32_bf16 v[68:71], v[228:231], v[32:35], v[68:71]
	v_pk_max_i16 v117, v117, 0
	v_mfma_f32_16x16x32_bf16 v[60:63], v[228:231], v[36:39], v[60:63]
	v_pk_max_i16 v118, v118, 0
	v_mfma_f32_16x16x32_bf16 v[56:59], v[224:227], v[36:39], v[56:59]
	v_pk_max_i16 v119, v119, 0
	ds_read_b128 v[224:227], v121 offset:57344
	ds_read_b128 v[228:231], v121 offset:58368
	s_waitcnt lgkmcnt(6)
	v_mfma_f32_16x16x32_bf16 v[64:67], v[232:235], v[40:43], v[64:67]
	v_mfma_f32_16x16x32_bf16 v[68:71], v[236:239], v[40:43], v[68:71]
	s_mov_b32 m0, s35
	s_add_i32 s51, s50, 0x0
	v_mfma_f32_16x16x32_bf16 v[60:63], v[236:239], v[44:47], v[60:63]
	buffer_load_dwordx4 v125, s[36:39], s51 offen lds
	v_mfma_f32_16x16x32_bf16 v[56:59], v[232:235], v[44:47], v[56:59]
	ds_read_b128 v[232:235], v121 offset:59392
	ds_read_b128 v[236:239], v121 offset:60416
	s_waitcnt lgkmcnt(6)
	ds_read_b128 v[152:155], v183 offset:256
	ds_read_b128 v[156:159], v183 offset:320
	v_mfma_f32_16x16x32_bf16 v[64:67], v[240:243], v[48:51], v[64:67]
	v_mfma_f32_16x16x32_bf16 v[68:71], v[244:247], v[48:51], v[68:71]
	s_mov_b32 m0, s42
	s_add_i32 s51, s50, 0x2000
	v_mfma_f32_16x16x32_bf16 v[60:63], v[244:247], v[52:55], v[60:63]
	buffer_load_dwordx4 v125, s[36:39], s51 offen lds
	v_mfma_f32_16x16x32_bf16 v[56:59], v[240:243], v[52:55], v[56:59]
	ds_read_b128 v[240:243], v121 offset:61440
	ds_read_b128 v[244:247], v121 offset:62464
	s_waitcnt lgkmcnt(8)
	v_mfma_f32_16x16x32_bf16 v[64:67], v[248:251], v[112:115], v[64:67]
	v_mfma_f32_16x16x32_bf16 v[68:71], v[252:255], v[112:115], v[68:71]
	s_mov_b32 m0, s41
	s_add_i32 s51, s50, 0x4000
	v_mfma_f32_16x16x32_bf16 v[60:63], v[252:255], v[116:119], v[60:63]
	buffer_load_dwordx4 v125, s[36:39], s51 offen lds
	v_mfma_f32_16x16x32_bf16 v[56:59], v[248:251], v[116:119], v[56:59]
	ds_read_b128 v[248:251], v121 offset:63488
	ds_read_b128 v[252:255], v121 offset:64512
	s_setprio 1
	s_waitcnt lgkmcnt(8)
	v_mfma_f32_16x16x32_bf16 v[80:83], v[224:227], v[0:3], v[160:163]
	v_mfma_f32_16x16x32_bf16 v[76:79], v[228:231], v[0:3], v[164:167]
	s_mov_b32 m0, s40
	s_add_i32 s51, s50, 0x6000
	v_mfma_f32_16x16x32_bf16 v[72:75], v[228:231], v[4:7], v[164:167]
	buffer_load_dwordx4 v125, s[36:39], s51 offen lds
	v_mfma_f32_16x16x32_bf16 v[84:87], v[224:227], v[4:7], v[160:163]
	ds_read_b128 v[224:227], v126 offset:57344
	ds_read_b128 v[228:231], v126 offset:58368
	s_waitcnt lgkmcnt(8)
	v_mfma_f32_16x16x32_bf16 v[80:83], v[232:235], v[12:15], v[80:83]
	v_mfma_f32_16x16x32_bf16 v[76:79], v[236:239], v[12:15], v[76:79]
	v_mfma_f32_16x16x32_bf16 v[72:75], v[236:239], v[8:11], v[72:75]
	v_mfma_f32_16x16x32_bf16 v[84:87], v[232:235], v[8:11], v[84:87]
	ds_read_b128 v[232:235], v126 offset:59392
	ds_read_b128 v[236:239], v126 offset:60416
	s_waitcnt lgkmcnt(6)
	v_mfma_f32_16x16x32_bf16 v[80:83], v[240:243], v[16:19], v[80:83]
	v_cvt_pk_bf16_f32 v88, v64, v65
	v_mfma_f32_16x16x32_bf16 v[76:79], v[244:247], v[16:19], v[76:79]
	v_cvt_pk_bf16_f32 v89, v66, v67
	v_mfma_f32_16x16x32_bf16 v[72:75], v[244:247], v[20:23], v[72:75]
	v_cvt_pk_bf16_f32 v90, v68, v69
	v_mfma_f32_16x16x32_bf16 v[84:87], v[240:243], v[20:23], v[84:87]
	v_cvt_pk_bf16_f32 v91, v70, v71
	ds_read_b128 v[240:243], v126 offset:61440
	ds_read_b128 v[244:247], v126 offset:62464
	s_waitcnt lgkmcnt(6)
	v_mfma_f32_16x16x32_bf16 v[80:83], v[248:251], v[24:27], v[80:83]
	v_cvt_pk_bf16_f32 v92, v56, v57
	v_mfma_f32_16x16x32_bf16 v[76:79], v[252:255], v[24:27], v[76:79]
	v_cvt_pk_bf16_f32 v93, v58, v59
	v_mfma_f32_16x16x32_bf16 v[72:75], v[252:255], v[28:31], v[72:75]
	v_cvt_pk_bf16_f32 v94, v60, v61
	v_mfma_f32_16x16x32_bf16 v[84:87], v[248:251], v[28:31], v[84:87]
	v_cvt_pk_bf16_f32 v95, v62, v63
	ds_read_b128 v[248:251], v126 offset:63488
	ds_read_b128 v[252:255], v126 offset:64512
	s_setprio 0
	s_waitcnt lgkmcnt(6)
	v_mfma_f32_16x16x32_bf16 v[80:83], v[224:227], v[32:35], v[80:83]
	v_pk_max_i16 v88, v88, 0
	v_mfma_f32_16x16x32_bf16 v[76:79], v[228:231], v[32:35], v[76:79]
	v_pk_max_i16 v89, v89, 0
	v_mfma_f32_16x16x32_bf16 v[72:75], v[228:231], v[36:39], v[72:75]
	v_pk_max_i16 v90, v90, 0
	v_mfma_f32_16x16x32_bf16 v[84:87], v[224:227], v[36:39], v[84:87]
	v_pk_max_i16 v91, v91, 0
	s_waitcnt lgkmcnt(4)
	v_mfma_f32_16x16x32_bf16 v[80:83], v[232:235], v[40:43], v[80:83]
	v_pk_max_i16 v92, v92, 0
	v_mfma_f32_16x16x32_bf16 v[76:79], v[236:239], v[40:43], v[76:79]
	v_pk_max_i16 v93, v93, 0
	v_mfma_f32_16x16x32_bf16 v[72:75], v[236:239], v[44:47], v[72:75]
	v_pk_max_i16 v94, v94, 0
	v_mfma_f32_16x16x32_bf16 v[84:87], v[232:235], v[44:47], v[84:87]
	v_pk_max_i16 v95, v95, 0
	s_branch .Lnerf_hid_b1
.Lnerf_hid_b0:
	s_waitcnt vmcnt(0) lgkmcnt(0)
	s_barrier
	ds_read_b128 v[224:227], v121 offset:40960
	ds_read_b128 v[228:231], v121 offset:41984
	v_mfma_f32_16x16x32_bf16 v[80:83], v[240:243], v[208:211], v[80:83]
	ds_read_b128 v[232:235], v121 offset:43008
	v_mfma_f32_16x16x32_bf16 v[76:79], v[244:247], v[208:211], v[76:79]
	ds_read_b128 v[236:239], v121 offset:44032
	v_mfma_f32_16x16x32_bf16 v[72:75], v[244:247], v[212:215], v[72:75]
	v_mfma_f32_16x16x32_bf16 v[84:87], v[240:243], v[212:215], v[84:87]
	ds_read_b128 v[240:243], v121 offset:45056
	ds_read_b128 v[244:247], v121 offset:46080
	v_mfma_f32_16x16x32_bf16 v[80:83], v[248:251], v[216:219], v[80:83]
	v_mfma_f32_16x16x32_bf16 v[76:79], v[252:255], v[216:219], v[76:79]
	v_mfma_f32_16x16x32_bf16 v[72:75], v[252:255], v[220:223], v[72:75]
	v_mfma_f32_16x16x32_bf16 v[84:87], v[248:251], v[220:223], v[84:87]
	ds_read_b128 v[248:251], v121 offset:47104
	ds_read_b128 v[252:255], v121 offset:48128
	s_setprio 3
	s_waitcnt lgkmcnt(6)
	v_mfma_f32_16x16x32_bf16 v[64:67], v[224:227], v[0:3], v[152:155]
	v_mfma_f32_16x16x32_bf16 v[68:71], v[228:231], v[0:3], v[156:159]
	v_mfma_f32_16x16x32_bf16 v[60:63], v[228:231], v[4:7], v[156:159]
	v_mfma_f32_16x16x32_bf16 v[56:59], v[224:227], v[4:7], v[152:155]
	ds_read_b128 v[224:227], v121 offset:49152
	ds_read_b128 v[228:231], v121 offset:50176
	s_waitcnt lgkmcnt(6)
	ds_read_b128 v[160:163], v183 offset:128
	ds_read_b128 v[164:167], v183 offset:192
	v_mfma_f32_16x16x32_bf16 v[64:67], v[232:235], v[12:15], v[64:67]
	v_cvt_pk_bf16_f32 v112, v80, v81
	v_mfma_f32_16x16x32_bf16 v[68:71], v[236:239], v[12:15], v[68:71]
	v_cvt_pk_bf16_f32 v113, v82, v83
	v_mfma_f32_16x16x32_bf16 v[60:63], v[236:239], v[8:11], v[60:63]
	v_cvt_pk_bf16_f32 v114, v76, v77
	v_mfma_f32_16x16x32_bf16 v[56:59], v[232:235], v[8:11], v[56:59]
	v_cvt_pk_bf16_f32 v115, v78, v79
	ds_read_b128 v[232:235], v121 offset:51200
	ds_read_b128 v[236:239], v121 offset:52224
	s_waitcnt lgkmcnt(8)
	v_mfma_f32_16x16x32_bf16 v[64:67], v[240:243], v[16:19], v[64:67]
	v_cvt_pk_bf16_f32 v116, v84, v85
	v_mfma_f32_16x16x32_bf16 v[68:71], v[244:247], v[16:19], v[68:71]
	v_cvt_pk_bf16_f32 v117, v86, v87
	v_mfma_f32_16x16x32_bf16 v[60:63], v[244:247], v[20:23], v[60:63]
	v_cvt_pk_bf16_f32 v118, v72, v73
	v_mfma_f32_16x16x32_bf16 v[56:59], v[240:243], v[20:23], v[56:59]
	v_cvt_pk_bf16_f32 v119, v74, v75
	ds_read_b128 v[240:243], v121 offset:53248
	ds_read_b128 v[244:247], v121 offset:54272
	s_waitcnt lgkmcnt(8)
	v_mfma_f32_16x16x32_bf16 v[64:67], v[248:251], v[24:27], v[64:67]
	v_pk_max_i16 v112, v112, 0
	v_mfma_f32_16x16x32_bf16 v[68:71], v[252:255], v[24:27], v[68:71]
	v_pk_max_i16 v113, v113, 0
	v_mfma_f32_16x16x32_bf16 v[60:63], v[252:255], v[28:31], v[60:63]
	v_pk_max_i16 v114, v114, 0
	v_mfma_f32_16x16x32_bf16 v[56:59], v[248:251], v[28:31], v[56:59]
	v_pk_max_i16 v115, v115, 0
	ds_read_b128 v[248:251], v121 offset:55296
	ds_read_b128 v[252:255], v121 offset:56320
	s_setprio 2
	s_waitcnt lgkmcnt(8)
	v_mfma_f32_16x16x32_bf16 v[64:67], v[224:227], v[32:35], v[64:67]
	v_pk_max_i16 v116, v116, 0
	v_mfma_f32_16x16x32_bf16 v[68:71], v[228:231], v[32:35], v[68:71]
	v_pk_max_i16 v117, v117, 0
	v_mfma_f32_16x16x32_bf16 v[60:63], v[228:231], v[36:39], v[60:63]
	v_pk_max_i16 v118, v118, 0
	v_mfma_f32_16x16x32_bf16 v[56:59], v[224:227], v[36:39], v[56:59]
	v_pk_max_i16 v119, v119, 0
	ds_read_b128 v[224:227], v121 offset:57344
	ds_read_b128 v[228:231], v121 offset:58368
	s_waitcnt lgkmcnt(6)
	v_mfma_f32_16x16x32_bf16 v[64:67], v[232:235], v[40:43], v[64:67]
	v_mfma_f32_16x16x32_bf16 v[68:71], v[236:239], v[40:43], v[68:71]
	s_mov_b32 m0, s35
	s_add_i32 s51, s50, 0x0
	v_mfma_f32_16x16x32_bf16 v[60:63], v[236:239], v[44:47], v[60:63]
	buffer_load_dwordx4 v125, s[36:39], s51 offen lds
	v_mfma_f32_16x16x32_bf16 v[56:59], v[232:235], v[44:47], v[56:59]
	ds_read_b128 v[232:235], v121 offset:59392
	ds_read_b128 v[236:239], v121 offset:60416
	s_waitcnt lgkmcnt(6)
	ds_read_b128 v[152:155], v183 offset:256
	ds_read_b128 v[156:159], v183 offset:320
	v_mfma_f32_16x16x32_bf16 v[64:67], v[240:243], v[48:51], v[64:67]
	v_mfma_f32_16x16x32_bf16 v[68:71], v[244:247], v[48:51], v[68:71]
	s_mov_b32 m0, s42
	s_add_i32 s51, s50, 0x2000
	v_mfma_f32_16x16x32_bf16 v[60:63], v[244:247], v[52:55], v[60:63]
	buffer_load_dwordx4 v125, s[36:39], s51 offen lds
	v_mfma_f32_16x16x32_bf16 v[56:59], v[240:243], v[52:55], v[56:59]
	ds_read_b128 v[240:243], v121 offset:61440
	ds_read_b128 v[244:247], v121 offset:62464
	s_waitcnt lgkmcnt(8)
	v_mfma_f32_16x16x32_bf16 v[64:67], v[248:251], v[112:115], v[64:67]
	v_mfma_f32_16x16x32_bf16 v[68:71], v[252:255], v[112:115], v[68:71]
	s_mov_b32 m0, s41
	s_add_i32 s51, s50, 0x4000
	v_mfma_f32_16x16x32_bf16 v[60:63], v[252:255], v[116:119], v[60:63]
	buffer_load_dwordx4 v125, s[36:39], s51 offen lds
	v_mfma_f32_16x16x32_bf16 v[56:59], v[248:251], v[116:119], v[56:59]
	ds_read_b128 v[248:251], v121 offset:63488
	ds_read_b128 v[252:255], v121 offset:64512
	s_setprio 1
	s_waitcnt lgkmcnt(8)
	v_mfma_f32_16x16x32_bf16 v[80:83], v[224:227], v[0:3], v[160:163]
	v_mfma_f32_16x16x32_bf16 v[76:79], v[228:231], v[0:3], v[164:167]
	s_mov_b32 m0, s40
	s_add_i32 s51, s50, 0x6000
	v_mfma_f32_16x16x32_bf16 v[72:75], v[228:231], v[4:7], v[164:167]
	buffer_load_dwordx4 v125, s[36:39], s51 offen lds
	v_mfma_f32_16x16x32_bf16 v[84:87], v[224:227], v[4:7], v[160:163]
	ds_read_b128 v[224:227], v126 offset:57344
	ds_read_b128 v[228:231], v126 offset:58368
	s_waitcnt lgkmcnt(8)
	v_mfma_f32_16x16x32_bf16 v[80:83], v[232:235], v[12:15], v[80:83]
	v_mfma_f32_16x16x32_bf16 v[76:79], v[236:239], v[12:15], v[76:79]
	v_mfma_f32_16x16x32_bf16 v[72:75], v[236:239], v[8:11], v[72:75]
	v_mfma_f32_16x16x32_bf16 v[84:87], v[232:235], v[8:11], v[84:87]
	ds_read_b128 v[232:235], v126 offset:59392
	ds_read_b128 v[236:239], v126 offset:60416
	s_waitcnt lgkmcnt(6)
	v_mfma_f32_16x16x32_bf16 v[80:83], v[240:243], v[16:19], v[80:83]
	v_cvt_pk_bf16_f32 v88, v64, v65
	v_mfma_f32_16x16x32_bf16 v[76:79], v[244:247], v[16:19], v[76:79]
	v_cvt_pk_bf16_f32 v89, v66, v67
	v_mfma_f32_16x16x32_bf16 v[72:75], v[244:247], v[20:23], v[72:75]
	v_cvt_pk_bf16_f32 v90, v68, v69
	v_mfma_f32_16x16x32_bf16 v[84:87], v[240:243], v[20:23], v[84:87]
	v_cvt_pk_bf16_f32 v91, v70, v71
	ds_read_b128 v[240:243], v126 offset:61440
	ds_read_b128 v[244:247], v126 offset:62464
	s_waitcnt lgkmcnt(6)
	v_mfma_f32_16x16x32_bf16 v[80:83], v[248:251], v[24:27], v[80:83]
	v_cvt_pk_bf16_f32 v92, v56, v57
	v_mfma_f32_16x16x32_bf16 v[76:79], v[252:255], v[24:27], v[76:79]
	v_cvt_pk_bf16_f32 v93, v58, v59
	v_mfma_f32_16x16x32_bf16 v[72:75], v[252:255], v[28:31], v[72:75]
	v_cvt_pk_bf16_f32 v94, v60, v61
	v_mfma_f32_16x16x32_bf16 v[84:87], v[248:251], v[28:31], v[84:87]
	v_cvt_pk_bf16_f32 v95, v62, v63
	ds_read_b128 v[248:251], v126 offset:63488
	ds_read_b128 v[252:255], v126 offset:64512
	s_setprio 0
	s_waitcnt lgkmcnt(6)
	v_mfma_f32_16x16x32_bf16 v[80:83], v[224:227], v[32:35], v[80:83]
	v_pk_max_i16 v88, v88, 0
	v_mfma_f32_16x16x32_bf16 v[76:79], v[228:231], v[32:35], v[76:79]
	v_pk_max_i16 v89, v89, 0
	v_mfma_f32_16x16x32_bf16 v[72:75], v[228:231], v[36:39], v[72:75]
	v_pk_max_i16 v90, v90, 0
	v_mfma_f32_16x16x32_bf16 v[84:87], v[224:227], v[36:39], v[84:87]
	v_pk_max_i16 v91, v91, 0
	s_waitcnt lgkmcnt(4)
	v_mfma_f32_16x16x32_bf16 v[80:83], v[232:235], v[40:43], v[80:83]
	v_pk_max_i16 v92, v92, 0
	v_mfma_f32_16x16x32_bf16 v[76:79], v[236:239], v[40:43], v[76:79]
	v_pk_max_i16 v93, v93, 0
	v_mfma_f32_16x16x32_bf16 v[72:75], v[236:239], v[44:47], v[72:75]
	v_pk_max_i16 v94, v94, 0
	v_mfma_f32_16x16x32_bf16 v[84:87], v[232:235], v[44:47], v[84:87]
	v_pk_max_i16 v95, v95, 0
.Lnerf_hid_b1:
	s_waitcnt vmcnt(0) lgkmcnt(0)
	s_barrier
	ds_read_b128 v[224:227], v121 offset:8192
	ds_read_b128 v[228:231], v121 offset:9216
	v_mfma_f32_16x16x32_bf16 v[80:83], v[240:243], v[48:51], v[80:83]
	ds_read_b128 v[232:235], v121 offset:10240
	v_mfma_f32_16x16x32_bf16 v[76:79], v[244:247], v[48:51], v[76:79]
	ds_read_b128 v[236:239], v121 offset:11264
	v_mfma_f32_16x16x32_bf16 v[72:75], v[244:247], v[52:55], v[72:75]
	v_mfma_f32_16x16x32_bf16 v[84:87], v[240:243], v[52:55], v[84:87]
	ds_read_b128 v[240:243], v121 offset:12288
	ds_read_b128 v[244:247], v121 offset:13312
	v_mfma_f32_16x16x32_bf16 v[80:83], v[248:251], v[112:115], v[80:83]
	v_mfma_f32_16x16x32_bf16 v[76:79], v[252:255], v[112:115], v[76:79]
	v_mfma_f32_16x16x32_bf16 v[72:75], v[252:255], v[116:119], v[72:75]
	v_mfma_f32_16x16x32_bf16 v[84:87], v[248:251], v[116:119], v[84:87]
	ds_read_b128 v[248:251], v121 offset:14336
	ds_read_b128 v[252:255], v121 offset:15360
	s_setprio 3
	s_waitcnt lgkmcnt(6)
	v_mfma_f32_16x16x32_bf16 v[64:67], v[224:227], v[0:3], v[152:155]
	v_mfma_f32_16x16x32_bf16 v[68:71], v[228:231], v[0:3], v[156:159]
	v_mfma_f32_16x16x32_bf16 v[60:63], v[228:231], v[4:7], v[156:159]
	v_mfma_f32_16x16x32_bf16 v[56:59], v[224:227], v[4:7], v[152:155]
	ds_read_b128 v[224:227], v121 offset:16384
	ds_read_b128 v[228:231], v121 offset:17408
	s_waitcnt lgkmcnt(6)
	ds_read_b128 v[160:163], v183 offset:384
	ds_read_b128 v[164:167], v183 offset:448
	v_mfma_f32_16x16x32_bf16 v[64:67], v[232:235], v[12:15], v[64:67]
	v_cvt_pk_bf16_f32 v96, v80, v81
	v_mfma_f32_16x16x32_bf16 v[68:71], v[236:239], v[12:15], v[68:71]
	v_cvt_pk_bf16_f32 v97, v82, v83
	v_mfma_f32_16x16x32_bf16 v[60:63], v[236:239], v[8:11], v[60:63]
	v_cvt_pk_bf16_f32 v98, v76, v77
	v_mfma_f32_16x16x32_bf16 v[56:59], v[232:235], v[8:11], v[56:59]
	v_cvt_pk_bf16_f32 v99, v78, v79
	ds_read_b128 v[232:235], v121 offset:18432
	ds_read_b128 v[236:239], v121 offset:19456
	s_waitcnt lgkmcnt(8)
	v_mfma_f32_16x16x32_bf16 v[64:67], v[240:243], v[16:19], v[64:67]
	v_cvt_pk_bf16_f32 v100, v84, v85
	v_mfma_f32_16x16x32_bf16 v[68:71], v[244:247], v[16:19], v[68:71]
	v_cvt_pk_bf16_f32 v101, v86, v87
	v_mfma_f32_16x16x32_bf16 v[60:63], v[244:247], v[20:23], v[60:63]
	v_cvt_pk_bf16_f32 v102, v72, v73
	v_mfma_f32_16x16x32_bf16 v[56:59], v[240:243], v[20:23], v[56:59]
	v_cvt_pk_bf16_f32 v103, v74, v75
	ds_read_b128 v[240:243], v121 offset:20480
	ds_read_b128 v[244:247], v121 offset:21504
	s_waitcnt lgkmcnt(8)
	v_mfma_f32_16x16x32_bf16 v[64:67], v[248:251], v[24:27], v[64:67]
	v_pk_max_i16 v96, v96, 0
	v_mfma_f32_16x16x32_bf16 v[68:71], v[252:255], v[24:27], v[68:71]
	v_pk_max_i16 v97, v97, 0
	v_mfma_f32_16x16x32_bf16 v[60:63], v[252:255], v[28:31], v[60:63]
	v_pk_max_i16 v98, v98, 0
	v_mfma_f32_16x16x32_bf16 v[56:59], v[248:251], v[28:31], v[56:59]
	v_pk_max_i16 v99, v99, 0
	ds_read_b128 v[248:251], v121 offset:22528
	ds_read_b128 v[252:255], v121 offset:23552
	s_setprio 2
	s_waitcnt lgkmcnt(8)
	v_mfma_f32_16x16x32_bf16 v[64:67], v[224:227], v[32:35], v[64:67]
	v_pk_max_i16 v100, v100, 0
	v_mfma_f32_16x16x32_bf16 v[68:71], v[228:231], v[32:35], v[68:71]
	v_pk_max_i16 v101, v101, 0
	v_mfma_f32_16x16x32_bf16 v[60:63], v[228:231], v[36:39], v[60:63]
	v_pk_max_i16 v102, v102, 0
	v_mfma_f32_16x16x32_bf16 v[56:59], v[224:227], v[36:39], v[56:59]
	v_pk_max_i16 v103, v103, 0
	ds_read_b128 v[224:227], v121 offset:24576
	ds_read_b128 v[228:231], v121 offset:25600
	s_waitcnt lgkmcnt(6)
	v_mfma_f32_16x16x32_bf16 v[64:67], v[232:235], v[40:43], v[64:67]
	v_mfma_f32_16x16x32_bf16 v[68:71], v[236:239], v[40:43], v[68:71]
	s_mov_b32 m0, s28
	s_add_i32 s51, s50, 0x8000
	v_mfma_f32_16x16x32_bf16 v[60:63], v[236:239], v[44:47], v[60:63]
	buffer_load_dwordx4 v125, s[36:39], s51 offen lds
	v_mfma_f32_16x16x32_bf16 v[56:59], v[232:235], v[44:47], v[56:59]
	ds_read_b128 v[232:235], v121 offset:26624
	ds_read_b128 v[236:239], v121 offset:27648
	s_waitcnt lgkmcnt(6)
	ds_read_b128 v[152:155], v183 offset:512
	ds_read_b128 v[156:159], v183 offset:576
	v_mfma_f32_16x16x32_bf16 v[64:67], v[240:243], v[48:51], v[64:67]
	v_mfma_f32_16x16x32_bf16 v[68:71], v[244:247], v[48:51], v[68:71]
	s_mov_b32 m0, s29
	s_add_i32 s51, s50, 0xa000
	v_mfma_f32_16x16x32_bf16 v[60:63], v[244:247], v[52:55], v[60:63]
	buffer_load_dwordx4 v125, s[36:39], s51 offen lds
	v_mfma_f32_16x16x32_bf16 v[56:59], v[240:243], v[52:55], v[56:59]
	ds_read_b128 v[240:243], v121 offset:28672
	ds_read_b128 v[244:247], v121 offset:29696
	s_waitcnt lgkmcnt(8)
	v_mfma_f32_16x16x32_bf16 v[64:67], v[248:251], v[112:115], v[64:67]
	v_mfma_f32_16x16x32_bf16 v[68:71], v[252:255], v[112:115], v[68:71]
	s_mov_b32 m0, s33
	s_add_i32 s51, s50, 0xc000
	v_mfma_f32_16x16x32_bf16 v[60:63], v[252:255], v[116:119], v[60:63]
	buffer_load_dwordx4 v125, s[36:39], s51 offen lds
	v_mfma_f32_16x16x32_bf16 v[56:59], v[248:251], v[116:119], v[56:59]
	ds_read_b128 v[248:251], v121 offset:30720
	ds_read_b128 v[252:255], v121 offset:31744
	s_setprio 1
	s_waitcnt lgkmcnt(8)
	v_mfma_f32_16x16x32_bf16 v[80:83], v[224:227], v[0:3], v[160:163]
	v_mfma_f32_16x16x32_bf16 v[76:79], v[228:231], v[0:3], v[164:167]
	s_mov_b32 m0, s34
	s_add_i32 s51, s50, 0xe000
	v_mfma_f32_16x16x32_bf16 v[72:75], v[228:231], v[4:7], v[164:167]
	buffer_load_dwordx4 v125, s[36:39], s51 offen lds
	v_mfma_f32_16x16x32_bf16 v[84:87], v[224:227], v[4:7], v[160:163]
	ds_read_b128 v[224:227], v121 offset:32768
	ds_read_b128 v[228:231], v121 offset:33792
	s_waitcnt lgkmcnt(8)
	v_mfma_f32_16x16x32_bf16 v[80:83], v[232:235], v[12:15], v[80:83]
	v_mfma_f32_16x16x32_bf16 v[76:79], v[236:239], v[12:15], v[76:79]
	v_mfma_f32_16x16x32_bf16 v[72:75], v[236:239], v[8:11], v[72:75]
	v_mfma_f32_16x16x32_bf16 v[84:87], v[232:235], v[8:11], v[84:87]
	ds_read_b128 v[232:235], v121 offset:34816
	ds_read_b128 v[236:239], v121 offset:35840
	s_waitcnt lgkmcnt(6)
	v_mfma_f32_16x16x32_bf16 v[80:83], v[240:243], v[16:19], v[80:83]
	v_cvt_pk_bf16_f32 v104, v64, v65
	v_mfma_f32_16x16x32_bf16 v[76:79], v[244:247], v[16:19], v[76:79]
	v_cvt_pk_bf16_f32 v105, v66, v67
	v_mfma_f32_16x16x32_bf16 v[72:75], v[244:247], v[20:23], v[72:75]
	v_cvt_pk_bf16_f32 v106, v68, v69
	v_mfma_f32_16x16x32_bf16 v[84:87], v[240:243], v[20:23], v[84:87]
	v_cvt_pk_bf16_f32 v107, v70, v71
	ds_read_b128 v[240:243], v121 offset:36864
	ds_read_b128 v[244:247], v121 offset:37888
	s_waitcnt lgkmcnt(6)
	v_mfma_f32_16x16x32_bf16 v[80:83], v[248:251], v[24:27], v[80:83]
	v_cvt_pk_bf16_f32 v108, v56, v57
	v_mfma_f32_16x16x32_bf16 v[76:79], v[252:255], v[24:27], v[76:79]
	v_cvt_pk_bf16_f32 v109, v58, v59
	v_mfma_f32_16x16x32_bf16 v[72:75], v[252:255], v[28:31], v[72:75]
	v_cvt_pk_bf16_f32 v110, v60, v61
	v_mfma_f32_16x16x32_bf16 v[84:87], v[248:251], v[28:31], v[84:87]
	v_cvt_pk_bf16_f32 v111, v62, v63
	ds_read_b128 v[248:251], v121 offset:38912
	ds_read_b128 v[252:255], v121 offset:39936
	s_setprio 0
	s_waitcnt lgkmcnt(6)
	v_mfma_f32_16x16x32_bf16 v[80:83], v[224:227], v[32:35], v[80:83]
	v_pk_max_i16 v104, v104, 0
	v_mfma_f32_16x16x32_bf16 v[76:79], v[228:231], v[32:35], v[76:79]
	v_pk_max_i16 v105, v105, 0
	v_mfma_f32_16x16x32_bf16 v[72:75], v[228:231], v[36:39], v[72:75]
	v_pk_max_i16 v106, v106, 0
	v_mfma_f32_16x16x32_bf16 v[84:87], v[224:227], v[36:39], v[84:87]
	v_pk_max_i16 v107, v107, 0
	s_waitcnt lgkmcnt(4)
	v_mfma_f32_16x16x32_bf16 v[80:83], v[232:235], v[40:43], v[80:83]
	v_pk_max_i16 v108, v108, 0
	v_mfma_f32_16x16x32_bf16 v[76:79], v[236:239], v[40:43], v[76:79]
	v_pk_max_i16 v109, v109, 0
	v_mfma_f32_16x16x32_bf16 v[72:75], v[236:239], v[44:47], v[72:75]
	v_pk_max_i16 v110, v110, 0
	v_mfma_f32_16x16x32_bf16 v[84:87], v[232:235], v[44:47], v[84:87]
	v_pk_max_i16 v111, v111, 0
.Lnerf_hid_b2:
	s_waitcnt vmcnt(0) lgkmcnt(0)
	s_barrier
	ds_read_b128 v[224:227], v121 offset:40960
	ds_read_b128 v[228:231], v121 offset:41984
	v_mfma_f32_16x16x32_bf16 v[80:83], v[240:243], v[48:51], v[80:83]
	ds_read_b128 v[232:235], v121 offset:43008
	v_mfma_f32_16x16x32_bf16 v[76:79], v[244:247], v[48:51], v[76:79]
	ds_read_b128 v[236:239], v121 offset:44032
	v_mfma_f32_16x16x32_bf16 v[72:75], v[244:247], v[52:55], v[72:75]
	v_mfma_f32_16x16x32_bf16 v[84:87], v[240:243], v[52:55], v[84:87]
	ds_read_b128 v[240:243], v121 offset:45056
	ds_read_b128 v[244:247], v121 offset:46080
	v_mfma_f32_16x16x32_bf16 v[80:83], v[248:251], v[112:115], v[80:83]
	v_mfma_f32_16x16x32_bf16 v[76:79], v[252:255], v[112:115], v[76:79]
	v_mfma_f32_16x16x32_bf16 v[72:75], v[252:255], v[116:119], v[72:75]
	v_mfma_f32_16x16x32_bf16 v[84:87], v[248:251], v[116:119], v[84:87]
	ds_read_b128 v[248:251], v121 offset:47104
	ds_read_b128 v[252:255], v121 offset:48128
	s_setprio 3
	s_waitcnt lgkmcnt(6)
	v_mfma_f32_16x16x32_bf16 v[64:67], v[224:227], v[0:3], v[152:155]
	v_mfma_f32_16x16x32_bf16 v[68:71], v[228:231], v[0:3], v[156:159]
	v_mfma_f32_16x16x32_bf16 v[60:63], v[228:231], v[4:7], v[156:159]
	v_mfma_f32_16x16x32_bf16 v[56:59], v[224:227], v[4:7], v[152:155]
	ds_read_b128 v[224:227], v121 offset:49152
	ds_read_b128 v[228:231], v121 offset:50176
	s_waitcnt lgkmcnt(6)
	ds_read_b128 v[160:163], v183 offset:640
	ds_read_b128 v[164:167], v183 offset:704
	v_mfma_f32_16x16x32_bf16 v[64:67], v[232:235], v[12:15], v[64:67]
	v_cvt_pk_bf16_f32 v184, v80, v81
	v_mfma_f32_16x16x32_bf16 v[68:71], v[236:239], v[12:15], v[68:71]
	v_cvt_pk_bf16_f32 v185, v82, v83
	v_mfma_f32_16x16x32_bf16 v[60:63], v[236:239], v[8:11], v[60:63]
	v_cvt_pk_bf16_f32 v186, v76, v77
	v_mfma_f32_16x16x32_bf16 v[56:59], v[232:235], v[8:11], v[56:59]
	v_cvt_pk_bf16_f32 v187, v78, v79
	ds_read_b128 v[232:235], v121 offset:51200
	ds_read_b128 v[236:239], v121 offset:52224
	s_waitcnt lgkmcnt(8)
	v_mfma_f32_16x16x32_bf16 v[64:67], v[240:243], v[16:19], v[64:67]
	v_cvt_pk_bf16_f32 v188, v84, v85
	v_mfma_f32_16x16x32_bf16 v[68:71], v[244:247], v[16:19], v[68:71]
	v_cvt_pk_bf16_f32 v189, v86, v87
	v_mfma_f32_16x16x32_bf16 v[60:63], v[244:247], v[20:23], v[60:63]
	v_cvt_pk_bf16_f32 v190, v72, v73
	v_mfma_f32_16x16x32_bf16 v[56:59], v[240:243], v[20:23], v[56:59]
	v_cvt_pk_bf16_f32 v191, v74, v75
	ds_read_b128 v[240:243], v121 offset:53248
	ds_read_b128 v[244:247], v121 offset:54272
	s_waitcnt lgkmcnt(8)
	v_mfma_f32_16x16x32_bf16 v[64:67], v[248:251], v[24:27], v[64:67]
	v_pk_max_i16 v184, v184, 0
	v_mfma_f32_16x16x32_bf16 v[68:71], v[252:255], v[24:27], v[68:71]
	v_pk_max_i16 v185, v185, 0
	v_mfma_f32_16x16x32_bf16 v[60:63], v[252:255], v[28:31], v[60:63]
	v_pk_max_i16 v186, v186, 0
	v_mfma_f32_16x16x32_bf16 v[56:59], v[248:251], v[28:31], v[56:59]
	v_pk_max_i16 v187, v187, 0
	ds_read_b128 v[248:251], v121 offset:55296
	ds_read_b128 v[252:255], v121 offset:56320
	s_setprio 2
	s_waitcnt lgkmcnt(8)
	v_mfma_f32_16x16x32_bf16 v[64:67], v[224:227], v[32:35], v[64:67]
	v_pk_max_i16 v188, v188, 0
	v_mfma_f32_16x16x32_bf16 v[68:71], v[228:231], v[32:35], v[68:71]
	v_pk_max_i16 v189, v189, 0
	v_mfma_f32_16x16x32_bf16 v[60:63], v[228:231], v[36:39], v[60:63]
	v_pk_max_i16 v190, v190, 0
	v_mfma_f32_16x16x32_bf16 v[56:59], v[224:227], v[36:39], v[56:59]
	v_pk_max_i16 v191, v191, 0
	ds_read_b128 v[224:227], v121 offset:57344
	ds_read_b128 v[228:231], v121 offset:58368
	s_waitcnt lgkmcnt(6)
	v_mfma_f32_16x16x32_bf16 v[64:67], v[232:235], v[40:43], v[64:67]
	v_mfma_f32_16x16x32_bf16 v[68:71], v[236:239], v[40:43], v[68:71]
	s_mov_b32 m0, s35
	s_add_i32 s51, s50, 0x10000
	v_mfma_f32_16x16x32_bf16 v[60:63], v[236:239], v[44:47], v[60:63]
	buffer_load_dwordx4 v125, s[36:39], s51 offen lds
	v_mfma_f32_16x16x32_bf16 v[56:59], v[232:235], v[44:47], v[56:59]
	ds_read_b128 v[232:235], v121 offset:59392
	ds_read_b128 v[236:239], v121 offset:60416
	s_waitcnt lgkmcnt(6)
	ds_read_b128 v[152:155], v183 offset:768
	ds_read_b128 v[156:159], v183 offset:832
	v_mfma_f32_16x16x32_bf16 v[64:67], v[240:243], v[48:51], v[64:67]
	v_mfma_f32_16x16x32_bf16 v[68:71], v[244:247], v[48:51], v[68:71]
	s_mov_b32 m0, s42
	s_add_i32 s51, s50, 0x12000
	v_mfma_f32_16x16x32_bf16 v[60:63], v[244:247], v[52:55], v[60:63]
	buffer_load_dwordx4 v125, s[36:39], s51 offen lds
	v_mfma_f32_16x16x32_bf16 v[56:59], v[240:243], v[52:55], v[56:59]
	ds_read_b128 v[240:243], v121 offset:61440
	ds_read_b128 v[244:247], v121 offset:62464
	s_waitcnt lgkmcnt(8)
	v_mfma_f32_16x16x32_bf16 v[64:67], v[248:251], v[112:115], v[64:67]
	v_mfma_f32_16x16x32_bf16 v[68:71], v[252:255], v[112:115], v[68:71]
	s_mov_b32 m0, s41
	s_add_i32 s51, s50, 0x14000
	v_mfma_f32_16x16x32_bf16 v[60:63], v[252:255], v[116:119], v[60:63]
	buffer_load_dwordx4 v125, s[36:39], s51 offen lds
	v_mfma_f32_16x16x32_bf16 v[56:59], v[248:251], v[116:119], v[56:59]
	ds_read_b128 v[248:251], v121 offset:63488
	ds_read_b128 v[252:255], v121 offset:64512
	s_setprio 1
	s_waitcnt lgkmcnt(8)
	v_mfma_f32_16x16x32_bf16 v[80:83], v[224:227], v[0:3], v[160:163]
	v_mfma_f32_16x16x32_bf16 v[76:79], v[228:231], v[0:3], v[164:167]
	s_mov_b32 m0, s40
	s_add_i32 s51, s50, 0x16000
	v_mfma_f32_16x16x32_bf16 v[72:75], v[228:231], v[4:7], v[164:167]
	buffer_load_dwordx4 v125, s[36:39], s51 offen lds
	v_mfma_f32_16x16x32_bf16 v[84:87], v[224:227], v[4:7], v[160:163]
	ds_read_b128 v[224:227], v126 offset:57344
	ds_read_b128 v[228:231], v126 offset:58368
	s_waitcnt lgkmcnt(8)
	v_mfma_f32_16x16x32_bf16 v[80:83], v[232:235], v[12:15], v[80:83]
	v_mfma_f32_16x16x32_bf16 v[76:79], v[236:239], v[12:15], v[76:79]
	v_mfma_f32_16x16x32_bf16 v[72:75], v[236:239], v[8:11], v[72:75]
	v_mfma_f32_16x16x32_bf16 v[84:87], v[232:235], v[8:11], v[84:87]
	ds_read_b128 v[232:235], v126 offset:59392
	ds_read_b128 v[236:239], v126 offset:60416
	s_waitcnt lgkmcnt(6)
	v_mfma_f32_16x16x32_bf16 v[80:83], v[240:243], v[16:19], v[80:83]
	v_cvt_pk_bf16_f32 v192, v64, v65
	v_mfma_f32_16x16x32_bf16 v[76:79], v[244:247], v[16:19], v[76:79]
	v_cvt_pk_bf16_f32 v193, v66, v67
	v_mfma_f32_16x16x32_bf16 v[72:75], v[244:247], v[20:23], v[72:75]
	v_cvt_pk_bf16_f32 v194, v68, v69
	v_mfma_f32_16x16x32_bf16 v[84:87], v[240:243], v[20:23], v[84:87]
	v_cvt_pk_bf16_f32 v195, v70, v71
	ds_read_b128 v[240:243], v126 offset:61440
	ds_read_b128 v[244:247], v126 offset:62464
	s_waitcnt lgkmcnt(6)
	v_mfma_f32_16x16x32_bf16 v[80:83], v[248:251], v[24:27], v[80:83]
	v_cvt_pk_bf16_f32 v196, v56, v57
	v_mfma_f32_16x16x32_bf16 v[76:79], v[252:255], v[24:27], v[76:79]
	v_cvt_pk_bf16_f32 v197, v58, v59
	v_mfma_f32_16x16x32_bf16 v[72:75], v[252:255], v[28:31], v[72:75]
	v_cvt_pk_bf16_f32 v198, v60, v61
	v_mfma_f32_16x16x32_bf16 v[84:87], v[248:251], v[28:31], v[84:87]
	v_cvt_pk_bf16_f32 v199, v62, v63
	ds_read_b128 v[248:251], v126 offset:63488
	ds_read_b128 v[252:255], v126 offset:64512
	s_setprio 0
	s_waitcnt lgkmcnt(6)
	v_mfma_f32_16x16x32_bf16 v[80:83], v[224:227], v[32:35], v[80:83]
	v_pk_max_i16 v192, v192, 0
	v_mfma_f32_16x16x32_bf16 v[76:79], v[228:231], v[32:35], v[76:79]
	v_pk_max_i16 v193, v193, 0
	v_mfma_f32_16x16x32_bf16 v[72:75], v[228:231], v[36:39], v[72:75]
	v_pk_max_i16 v194, v194, 0
	v_mfma_f32_16x16x32_bf16 v[84:87], v[224:227], v[36:39], v[84:87]
	v_pk_max_i16 v195, v195, 0
	s_waitcnt lgkmcnt(4)
	v_mfma_f32_16x16x32_bf16 v[80:83], v[232:235], v[40:43], v[80:83]
	v_pk_max_i16 v196, v196, 0
	v_mfma_f32_16x16x32_bf16 v[76:79], v[236:239], v[40:43], v[76:79]
	v_pk_max_i16 v197, v197, 0
	v_mfma_f32_16x16x32_bf16 v[72:75], v[236:239], v[44:47], v[72:75]
	v_pk_max_i16 v198, v198, 0
	v_mfma_f32_16x16x32_bf16 v[84:87], v[232:235], v[44:47], v[84:87]
	v_pk_max_i16 v199, v199, 0
.Lnerf_hid_b3:
	s_waitcnt vmcnt(0) lgkmcnt(0)
	s_barrier
	ds_read_b128 v[224:227], v121 offset:8192
	ds_read_b128 v[228:231], v121 offset:9216
	v_mfma_f32_16x16x32_bf16 v[80:83], v[240:243], v[48:51], v[80:83]
	ds_read_b128 v[232:235], v121 offset:10240
	v_mfma_f32_16x16x32_bf16 v[76:79], v[244:247], v[48:51], v[76:79]
	ds_read_b128 v[236:239], v121 offset:11264
	v_mfma_f32_16x16x32_bf16 v[72:75], v[244:247], v[52:55], v[72:75]
	v_mfma_f32_16x16x32_bf16 v[84:87], v[240:243], v[52:55], v[84:87]
	ds_read_b128 v[240:243], v121 offset:12288
	ds_read_b128 v[244:247], v121 offset:13312
	v_mfma_f32_16x16x32_bf16 v[80:83], v[248:251], v[112:115], v[80:83]
	v_mfma_f32_16x16x32_bf16 v[76:79], v[252:255], v[112:115], v[76:79]
	v_mfma_f32_16x16x32_bf16 v[72:75], v[252:255], v[116:119], v[72:75]
	v_mfma_f32_16x16x32_bf16 v[84:87], v[248:251], v[116:119], v[84:87]
	ds_read_b128 v[248:251], v121 offset:14336
	ds_read_b128 v[252:255], v121 offset:15360
	s_setprio 3
	s_waitcnt lgkmcnt(6)
	v_mfma_f32_16x16x32_bf16 v[64:67], v[224:227], v[0:3], v[152:155]
	v_mfma_f32_16x16x32_bf16 v[68:71], v[228:231], v[0:3], v[156:159]
	v_mfma_f32_16x16x32_bf16 v[60:63], v[228:231], v[4:7], v[156:159]
	v_mfma_f32_16x16x32_bf16 v[56:59], v[224:227], v[4:7], v[152:155]
	ds_read_b128 v[224:227], v121 offset:16384
	ds_read_b128 v[228:231], v121 offset:17408
	s_waitcnt lgkmcnt(6)
	ds_read_b128 v[160:163], v183 offset:896
	ds_read_b128 v[164:167], v183 offset:960
	v_mfma_f32_16x16x32_bf16 v[64:67], v[232:235], v[12:15], v[64:67]
	v_cvt_pk_bf16_f32 v200, v80, v81
	v_mfma_f32_16x16x32_bf16 v[68:71], v[236:239], v[12:15], v[68:71]
	v_cvt_pk_bf16_f32 v201, v82, v83
	v_mfma_f32_16x16x32_bf16 v[60:63], v[236:239], v[8:11], v[60:63]
	v_cvt_pk_bf16_f32 v202, v76, v77
	v_mfma_f32_16x16x32_bf16 v[56:59], v[232:235], v[8:11], v[56:59]
	v_cvt_pk_bf16_f32 v203, v78, v79
	ds_read_b128 v[232:235], v121 offset:18432
	ds_read_b128 v[236:239], v121 offset:19456
	s_waitcnt lgkmcnt(8)
	v_mfma_f32_16x16x32_bf16 v[64:67], v[240:243], v[16:19], v[64:67]
	v_cvt_pk_bf16_f32 v204, v84, v85
	v_mfma_f32_16x16x32_bf16 v[68:71], v[244:247], v[16:19], v[68:71]
	v_cvt_pk_bf16_f32 v205, v86, v87
	v_mfma_f32_16x16x32_bf16 v[60:63], v[244:247], v[20:23], v[60:63]
	v_cvt_pk_bf16_f32 v206, v72, v73
	v_mfma_f32_16x16x32_bf16 v[56:59], v[240:243], v[20:23], v[56:59]
	v_cvt_pk_bf16_f32 v207, v74, v75
	ds_read_b128 v[240:243], v121 offset:20480
	ds_read_b128 v[244:247], v121 offset:21504
	s_waitcnt lgkmcnt(8)
	v_mfma_f32_16x16x32_bf16 v[64:67], v[248:251], v[24:27], v[64:67]
	v_pk_max_i16 v200, v200, 0
	v_mfma_f32_16x16x32_bf16 v[68:71], v[252:255], v[24:27], v[68:71]
	v_pk_max_i16 v201, v201, 0
	v_mfma_f32_16x16x32_bf16 v[60:63], v[252:255], v[28:31], v[60:63]
	v_pk_max_i16 v202, v202, 0
	v_mfma_f32_16x16x32_bf16 v[56:59], v[248:251], v[28:31], v[56:59]
	v_pk_max_i16 v203, v203, 0
	ds_read_b128 v[248:251], v121 offset:22528
	ds_read_b128 v[252:255], v121 offset:23552
	s_setprio 2
	s_waitcnt lgkmcnt(8)
	v_mfma_f32_16x16x32_bf16 v[64:67], v[224:227], v[32:35], v[64:67]
	v_pk_max_i16 v204, v204, 0
	v_mfma_f32_16x16x32_bf16 v[68:71], v[228:231], v[32:35], v[68:71]
	v_pk_max_i16 v205, v205, 0
	v_mfma_f32_16x16x32_bf16 v[60:63], v[228:231], v[36:39], v[60:63]
	v_pk_max_i16 v206, v206, 0
	v_mfma_f32_16x16x32_bf16 v[56:59], v[224:227], v[36:39], v[56:59]
	v_pk_max_i16 v207, v207, 0
	ds_read_b128 v[224:227], v121 offset:24576
	ds_read_b128 v[228:231], v121 offset:25600
	s_waitcnt lgkmcnt(6)
	v_mfma_f32_16x16x32_bf16 v[64:67], v[232:235], v[40:43], v[64:67]
	v_mfma_f32_16x16x32_bf16 v[68:71], v[236:239], v[40:43], v[68:71]
	s_mov_b32 m0, s28
	s_add_i32 s51, s50, 0x18000
	v_mfma_f32_16x16x32_bf16 v[60:63], v[236:239], v[44:47], v[60:63]
	buffer_load_dwordx4 v125, s[36:39], s51 offen lds
	v_mfma_f32_16x16x32_bf16 v[56:59], v[232:235], v[44:47], v[56:59]
	ds_read_b128 v[232:235], v121 offset:26624
	ds_read_b128 v[236:239], v121 offset:27648
	s_waitcnt lgkmcnt(6)
	ds_read_b128 v[152:155], v183 offset:1024
	ds_read_b128 v[156:159], v183 offset:1088
	v_mfma_f32_16x16x32_bf16 v[64:67], v[240:243], v[48:51], v[64:67]
	v_mfma_f32_16x16x32_bf16 v[68:71], v[244:247], v[48:51], v[68:71]
	s_mov_b32 m0, s29
	s_add_i32 s51, s50, 0x1a000
	v_mfma_f32_16x16x32_bf16 v[60:63], v[244:247], v[52:55], v[60:63]
	buffer_load_dwordx4 v125, s[36:39], s51 offen lds
	v_mfma_f32_16x16x32_bf16 v[56:59], v[240:243], v[52:55], v[56:59]
	ds_read_b128 v[240:243], v121 offset:28672
	ds_read_b128 v[244:247], v121 offset:29696
	s_waitcnt lgkmcnt(8)
	v_mfma_f32_16x16x32_bf16 v[64:67], v[248:251], v[112:115], v[64:67]
	v_mfma_f32_16x16x32_bf16 v[68:71], v[252:255], v[112:115], v[68:71]
	s_mov_b32 m0, s33
	s_add_i32 s51, s50, 0x1c000
	v_mfma_f32_16x16x32_bf16 v[60:63], v[252:255], v[116:119], v[60:63]
	buffer_load_dwordx4 v125, s[36:39], s51 offen lds
	v_mfma_f32_16x16x32_bf16 v[56:59], v[248:251], v[116:119], v[56:59]
	ds_read_b128 v[248:251], v121 offset:30720
	ds_read_b128 v[252:255], v121 offset:31744
	s_setprio 1
	s_waitcnt lgkmcnt(8)
	v_mfma_f32_16x16x32_bf16 v[80:83], v[224:227], v[0:3], v[160:163]
	v_mfma_f32_16x16x32_bf16 v[76:79], v[228:231], v[0:3], v[164:167]
	s_mov_b32 m0, s34
	s_add_i32 s51, s50, 0x1e000
	v_mfma_f32_16x16x32_bf16 v[72:75], v[228:231], v[4:7], v[164:167]
	buffer_load_dwordx4 v125, s[36:39], s51 offen lds
	v_mfma_f32_16x16x32_bf16 v[84:87], v[224:227], v[4:7], v[160:163]
	ds_read_b128 v[224:227], v121 offset:32768
	ds_read_b128 v[228:231], v121 offset:33792
	s_waitcnt lgkmcnt(8)
	v_mfma_f32_16x16x32_bf16 v[80:83], v[232:235], v[12:15], v[80:83]
	v_mfma_f32_16x16x32_bf16 v[76:79], v[236:239], v[12:15], v[76:79]
	v_mfma_f32_16x16x32_bf16 v[72:75], v[236:239], v[8:11], v[72:75]
	v_mfma_f32_16x16x32_bf16 v[84:87], v[232:235], v[8:11], v[84:87]
	ds_read_b128 v[232:235], v121 offset:34816
	ds_read_b128 v[236:239], v121 offset:35840
	s_waitcnt lgkmcnt(6)
	v_mfma_f32_16x16x32_bf16 v[80:83], v[240:243], v[16:19], v[80:83]
	v_cvt_pk_bf16_f32 v208, v64, v65
	v_mfma_f32_16x16x32_bf16 v[76:79], v[244:247], v[16:19], v[76:79]
	v_cvt_pk_bf16_f32 v209, v66, v67
	v_mfma_f32_16x16x32_bf16 v[72:75], v[244:247], v[20:23], v[72:75]
	v_cvt_pk_bf16_f32 v210, v68, v69
	v_mfma_f32_16x16x32_bf16 v[84:87], v[240:243], v[20:23], v[84:87]
	v_cvt_pk_bf16_f32 v211, v70, v71
	ds_read_b128 v[240:243], v121 offset:36864
	ds_read_b128 v[244:247], v121 offset:37888
	s_waitcnt lgkmcnt(6)
	v_mfma_f32_16x16x32_bf16 v[80:83], v[248:251], v[24:27], v[80:83]
	v_cvt_pk_bf16_f32 v212, v56, v57
	v_mfma_f32_16x16x32_bf16 v[76:79], v[252:255], v[24:27], v[76:79]
	v_cvt_pk_bf16_f32 v213, v58, v59
	v_mfma_f32_16x16x32_bf16 v[72:75], v[252:255], v[28:31], v[72:75]
	v_cvt_pk_bf16_f32 v214, v60, v61
	v_mfma_f32_16x16x32_bf16 v[84:87], v[248:251], v[28:31], v[84:87]
	v_cvt_pk_bf16_f32 v215, v62, v63
	ds_read_b128 v[248:251], v121 offset:38912
	ds_read_b128 v[252:255], v121 offset:39936
	s_setprio 0
	s_waitcnt lgkmcnt(6)
	v_mfma_f32_16x16x32_bf16 v[80:83], v[224:227], v[32:35], v[80:83]
	v_pk_max_i16 v208, v208, 0
	v_mfma_f32_16x16x32_bf16 v[76:79], v[228:231], v[32:35], v[76:79]
	v_pk_max_i16 v209, v209, 0
	v_mfma_f32_16x16x32_bf16 v[72:75], v[228:231], v[36:39], v[72:75]
	v_pk_max_i16 v210, v210, 0
	v_mfma_f32_16x16x32_bf16 v[84:87], v[224:227], v[36:39], v[84:87]
	v_pk_max_i16 v211, v211, 0
	s_waitcnt lgkmcnt(4)
	v_mfma_f32_16x16x32_bf16 v[80:83], v[232:235], v[40:43], v[80:83]
	v_pk_max_i16 v212, v212, 0
	v_mfma_f32_16x16x32_bf16 v[76:79], v[236:239], v[40:43], v[76:79]
	v_pk_max_i16 v213, v213, 0
	v_mfma_f32_16x16x32_bf16 v[72:75], v[236:239], v[44:47], v[72:75]
	v_pk_max_i16 v214, v214, 0
	v_mfma_f32_16x16x32_bf16 v[84:87], v[232:235], v[44:47], v[84:87]
	v_pk_max_i16 v215, v215, 0
	s_cmp_eq_u32 s52, 3
	s_cbranch_scc1 .Lnerf_head

.Lnerf_e2skip_2:
	s_waitcnt lgkmcnt(6)
	ds_read_b128 v[160:163], v183 offset:1152
	ds_read_b128 v[164:167], v183 offset:1216
	v_mfma_f32_16x16x32_bf16 v[64:67], v[232:235], v[96:99], v[64:67]
	v_cvt_pk_bf16_f32 v216, v80, v81
	v_mfma_f32_16x16x32_bf16 v[68:71], v[236:239], v[96:99], v[68:71]
	v_cvt_pk_bf16_f32 v217, v82, v83
	v_mfma_f32_16x16x32_bf16 v[60:63], v[236:239], v[100:103], v[60:63]
	v_cvt_pk_bf16_f32 v218, v76, v77
	v_mfma_f32_16x16x32_bf16 v[56:59], v[232:235], v[100:103], v[56:59]
	v_cvt_pk_bf16_f32 v219, v78, v79
	ds_read_b128 v[232:235], v121 offset:51200
	ds_read_b128 v[236:239], v121 offset:52224
	s_waitcnt lgkmcnt(8)
	v_mfma_f32_16x16x32_bf16 v[64:67], v[240:243], v[104:107], v[64:67]
	v_cvt_pk_bf16_f32 v220, v84, v85
	v_mfma_f32_16x16x32_bf16 v[68:71], v[244:247], v[104:107], v[68:71]
	v_cvt_pk_bf16_f32 v221, v86, v87
	v_mfma_f32_16x16x32_bf16 v[60:63], v[244:247], v[108:111], v[60:63]
	v_cvt_pk_bf16_f32 v222, v72, v73
	v_mfma_f32_16x16x32_bf16 v[56:59], v[240:243], v[108:111], v[56:59]
	v_cvt_pk_bf16_f32 v223, v74, v75
	ds_read_b128 v[240:243], v121 offset:53248
	ds_read_b128 v[244:247], v121 offset:54272
	s_waitcnt lgkmcnt(8)
	v_mfma_f32_16x16x32_bf16 v[64:67], v[248:251], v[184:187], v[64:67]
	v_pk_max_i16 v216, v216, 0
	v_mfma_f32_16x16x32_bf16 v[68:71], v[252:255], v[184:187], v[68:71]
	v_pk_max_i16 v217, v217, 0
	v_mfma_f32_16x16x32_bf16 v[60:63], v[252:255], v[188:191], v[60:63]
	v_pk_max_i16 v218, v218, 0
	v_mfma_f32_16x16x32_bf16 v[56:59], v[248:251], v[188:191], v[56:59]
	v_pk_max_i16 v219, v219, 0
	ds_read_b128 v[248:251], v121 offset:55296
	ds_read_b128 v[252:255], v121 offset:56320
	s_setprio 2
	s_waitcnt lgkmcnt(8)
	v_mfma_f32_16x16x32_bf16 v[64:67], v[224:227], v[192:195], v[64:67]
	v_pk_max_i16 v220, v220, 0
	v_mfma_f32_16x16x32_bf16 v[68:71], v[228:231], v[192:195], v[68:71]
	v_pk_max_i16 v221, v221, 0
	v_mfma_f32_16x16x32_bf16 v[60:63], v[228:231], v[196:199], v[60:63]
	v_pk_max_i16 v222, v222, 0
	v_mfma_f32_16x16x32_bf16 v[56:59], v[224:227], v[196:199], v[56:59]
	v_pk_max_i16 v223, v223, 0
	ds_read_b128 v[224:227], v121 offset:57344
	ds_read_b128 v[228:231], v121 offset:58368
	s_waitcnt lgkmcnt(6)
	v_mfma_f32_16x16x32_bf16 v[64:67], v[232:235], v[200:203], v[64:67]
	v_mfma_f32_16x16x32_bf16 v[68:71], v[236:239], v[200:203], v[68:71]
	s_mov_b32 m0, s35
	s_add_i32 s51, s50, 0x20000
	v_mfma_f32_16x16x32_bf16 v[60:63], v[236:239], v[204:207], v[60:63]
	buffer_load_dwordx4 v125, s[36:39], s51 offen lds
	v_mfma_f32_16x16x32_bf16 v[56:59], v[232:235], v[204:207], v[56:59]
	ds_read_b128 v[232:235], v121 offset:59392
	ds_read_b128 v[236:239], v121 offset:60416
	s_waitcnt lgkmcnt(6)
	ds_read_b128 v[152:155], v183 offset:1280
	ds_read_b128 v[156:159], v183 offset:1344
	v_mfma_f32_16x16x32_bf16 v[64:67], v[240:243], v[208:211], v[64:67]
	v_mfma_f32_16x16x32_bf16 v[68:71], v[244:247], v[208:211], v[68:71]
	s_mov_b32 m0, s42
	s_add_i32 s51, s50, 0x22000
	v_mfma_f32_16x16x32_bf16 v[60:63], v[244:247], v[212:215], v[60:63]
	buffer_load_dwordx4 v125, s[36:39], s51 offen lds
	v_mfma_f32_16x16x32_bf16 v[56:59], v[240:243], v[212:215], v[56:59]
	ds_read_b128 v[240:243], v121 offset:61440
	ds_read_b128 v[244:247], v121 offset:62464
	s_waitcnt lgkmcnt(8)
	v_mfma_f32_16x16x32_bf16 v[64:67], v[248:251], v[216:219], v[64:67]
	v_mfma_f32_16x16x32_bf16 v[68:71], v[252:255], v[216:219], v[68:71]
	s_mov_b32 m0, s41
	s_add_i32 s51, s50, 0x24000
	v_mfma_f32_16x16x32_bf16 v[60:63], v[252:255], v[220:223], v[60:63]
	buffer_load_dwordx4 v125, s[36:39], s51 offen lds
	v_mfma_f32_16x16x32_bf16 v[56:59], v[248:251], v[220:223], v[56:59]
	ds_read_b128 v[248:251], v121 offset:63488
	ds_read_b128 v[252:255], v121 offset:64512
	s_setprio 1
	s_waitcnt lgkmcnt(8)
	v_mfma_f32_16x16x32_bf16 v[80:83], v[224:227], v[88:91], v[160:163]
	v_mfma_f32_16x16x32_bf16 v[76:79], v[228:231], v[88:91], v[164:167]
	s_mov_b32 m0, s40
	s_add_i32 s51, s50, 0x26000
	v_mfma_f32_16x16x32_bf16 v[72:75], v[228:231], v[92:95], v[164:167]
	buffer_load_dwordx4 v125, s[36:39], s51 offen lds
	v_mfma_f32_16x16x32_bf16 v[84:87], v[224:227], v[92:95], v[160:163]
	ds_read_b128 v[224:227], v126 offset:57344
	ds_read_b128 v[228:231], v126 offset:58368
	s_waitcnt lgkmcnt(8)
	v_mfma_f32_16x16x32_bf16 v[80:83], v[232:235], v[96:99], v[80:83]
	v_mfma_f32_16x16x32_bf16 v[76:79], v[236:239], v[96:99], v[76:79]
	v_mfma_f32_16x16x32_bf16 v[72:75], v[236:239], v[100:103], v[72:75]
	v_mfma_f32_16x16x32_bf16 v[84:87], v[232:235], v[100:103], v[84:87]
	ds_read_b128 v[232:235], v126 offset:59392
	ds_read_b128 v[236:239], v126 offset:60416
	s_waitcnt lgkmcnt(6)
	v_mfma_f32_16x16x32_bf16 v[80:83], v[240:243], v[104:107], v[80:83]
	v_cvt_pk_bf16_f32 v0, v64, v65
	v_mfma_f32_16x16x32_bf16 v[76:79], v[244:247], v[104:107], v[76:79]
	v_cvt_pk_bf16_f32 v1, v66, v67
	v_mfma_f32_16x16x32_bf16 v[72:75], v[244:247], v[108:111], v[72:75]
	v_cvt_pk_bf16_f32 v2, v68, v69
	v_mfma_f32_16x16x32_bf16 v[84:87], v[240:243], v[108:111], v[84:87]
	v_cvt_pk_bf16_f32 v3, v70, v71
	ds_read_b128 v[240:243], v126 offset:61440
	ds_read_b128 v[244:247], v126 offset:62464
	s_waitcnt lgkmcnt(6)
	v_mfma_f32_16x16x32_bf16 v[80:83], v[248:251], v[184:187], v[80:83]
	v_cvt_pk_bf16_f32 v4, v56, v57
	v_mfma_f32_16x16x32_bf16 v[76:79], v[252:255], v[184:187], v[76:79]
	v_cvt_pk_bf16_f32 v5, v58, v59
	v_mfma_f32_16x16x32_bf16 v[72:75], v[252:255], v[188:191], v[72:75]
	v_cvt_pk_bf16_f32 v6, v60, v61
	v_mfma_f32_16x16x32_bf16 v[84:87], v[248:251], v[188:191], v[84:87]
	v_cvt_pk_bf16_f32 v7, v62, v63
	ds_read_b128 v[248:251], v126 offset:63488
	ds_read_b128 v[252:255], v126 offset:64512
	s_setprio 0
	s_waitcnt lgkmcnt(6)
	v_mfma_f32_16x16x32_bf16 v[80:83], v[224:227], v[192:195], v[80:83]
	v_pk_max_i16 v0, v0, 0
	v_mfma_f32_16x16x32_bf16 v[76:79], v[228:231], v[192:195], v[76:79]
	v_pk_max_i16 v1, v1, 0
	v_mfma_f32_16x16x32_bf16 v[72:75], v[228:231], v[196:199], v[72:75]
	v_pk_max_i16 v2, v2, 0
	v_mfma_f32_16x16x32_bf16 v[84:87], v[224:227], v[196:199], v[84:87]
	v_pk_max_i16 v3, v3, 0
	s_waitcnt lgkmcnt(4)
	v_mfma_f32_16x16x32_bf16 v[80:83], v[232:235], v[200:203], v[80:83]
	v_pk_max_i16 v4, v4, 0
	v_mfma_f32_16x16x32_bf16 v[76:79], v[236:239], v[200:203], v[76:79]
	v_pk_max_i16 v5, v5, 0
	v_mfma_f32_16x16x32_bf16 v[72:75], v[236:239], v[204:207], v[72:75]
	v_pk_max_i16 v6, v6, 0
	v_mfma_f32_16x16x32_bf16 v[84:87], v[232:235], v[204:207], v[84:87]
	v_pk_max_i16 v7, v7, 0
.Lnerf_hid_b5:
	s_waitcnt vmcnt(0) lgkmcnt(0)
	s_barrier
	ds_read_b128 v[224:227], v121 offset:8192
	ds_read_b128 v[228:231], v121 offset:9216
	v_mfma_f32_16x16x32_bf16 v[80:83], v[240:243], v[208:211], v[80:83]
	ds_read_b128 v[232:235], v121 offset:10240
	v_mfma_f32_16x16x32_bf16 v[76:79], v[244:247], v[208:211], v[76:79]
	ds_read_b128 v[236:239], v121 offset:11264
	v_mfma_f32_16x16x32_bf16 v[72:75], v[244:247], v[212:215], v[72:75]
	v_mfma_f32_16x16x32_bf16 v[84:87], v[240:243], v[212:215], v[84:87]
	ds_read_b128 v[240:243], v121 offset:12288
	ds_read_b128 v[244:247], v121 offset:13312
	v_mfma_f32_16x16x32_bf16 v[80:83], v[248:251], v[216:219], v[80:83]
	v_mfma_f32_16x16x32_bf16 v[76:79], v[252:255], v[216:219], v[76:79]
	v_mfma_f32_16x16x32_bf16 v[72:75], v[252:255], v[220:223], v[72:75]
	v_mfma_f32_16x16x32_bf16 v[84:87], v[248:251], v[220:223], v[84:87]
	ds_read_b128 v[248:251], v121 offset:14336
	ds_read_b128 v[252:255], v121 offset:15360
	s_setprio 3
	s_waitcnt lgkmcnt(6)
	v_mfma_f32_16x16x32_bf16 v[64:67], v[224:227], v[88:91], v[152:155]
	v_mfma_f32_16x16x32_bf16 v[68:71], v[228:231], v[88:91], v[156:159]
	v_mfma_f32_16x16x32_bf16 v[60:63], v[228:231], v[92:95], v[156:159]
	v_mfma_f32_16x16x32_bf16 v[56:59], v[224:227], v[92:95], v[152:155]
	ds_read_b128 v[224:227], v121 offset:16384
	ds_read_b128 v[228:231], v121 offset:17408
	s_waitcnt lgkmcnt(6)
	ds_read_b128 v[160:163], v183 offset:1408
	ds_read_b128 v[164:167], v183 offset:1472
	v_mfma_f32_16x16x32_bf16 v[64:67], v[232:235], v[96:99], v[64:67]
	v_cvt_pk_bf16_f32 v12, v80, v81
	v_mfma_f32_16x16x32_bf16 v[68:71], v[236:239], v[96:99], v[68:71]
	v_cvt_pk_bf16_f32 v13, v82, v83
	v_mfma_f32_16x16x32_bf16 v[60:63], v[236:239], v[100:103], v[60:63]
	v_cvt_pk_bf16_f32 v14, v76, v77
	v_mfma_f32_16x16x32_bf16 v[56:59], v[232:235], v[100:103], v[56:59]
	v_cvt_pk_bf16_f32 v15, v78, v79
	ds_read_b128 v[232:235], v121 offset:18432
	ds_read_b128 v[236:239], v121 offset:19456
	s_waitcnt lgkmcnt(8)
	v_mfma_f32_16x16x32_bf16 v[64:67], v[240:243], v[104:107], v[64:67]
	v_cvt_pk_bf16_f32 v8, v84, v85
	v_mfma_f32_16x16x32_bf16 v[68:71], v[244:247], v[104:107], v[68:71]
	v_cvt_pk_bf16_f32 v9, v86, v87
	v_mfma_f32_16x16x32_bf16 v[60:63], v[244:247], v[108:111], v[60:63]
	v_cvt_pk_bf16_f32 v10, v72, v73
	v_mfma_f32_16x16x32_bf16 v[56:59], v[240:243], v[108:111], v[56:59]
	v_cvt_pk_bf16_f32 v11, v74, v75
	ds_read_b128 v[240:243], v121 offset:20480
	ds_read_b128 v[244:247], v121 offset:21504
	s_waitcnt lgkmcnt(8)
	v_mfma_f32_16x16x32_bf16 v[64:67], v[248:251], v[184:187], v[64:67]
	v_pk_max_i16 v12, v12, 0
	v_mfma_f32_16x16x32_bf16 v[68:71], v[252:255], v[184:187], v[68:71]
	v_pk_max_i16 v13, v13, 0
	v_mfma_f32_16x16x32_bf16 v[60:63], v[252:255], v[188:191], v[60:63]
	v_pk_max_i16 v14, v14, 0
	v_mfma_f32_16x16x32_bf16 v[56:59], v[248:251], v[188:191], v[56:59]
	v_pk_max_i16 v15, v15, 0
	ds_read_b128 v[248:251], v121 offset:22528
	ds_read_b128 v[252:255], v121 offset:23552
	s_setprio 2
	s_waitcnt lgkmcnt(8)
	v_mfma_f32_16x16x32_bf16 v[64:67], v[224:227], v[192:195], v[64:67]
	v_pk_max_i16 v8, v8, 0
	v_mfma_f32_16x16x32_bf16 v[68:71], v[228:231], v[192:195], v[68:71]
	v_pk_max_i16 v9, v9, 0
	v_mfma_f32_16x16x32_bf16 v[60:63], v[228:231], v[196:199], v[60:63]
	v_pk_max_i16 v10, v10, 0
	v_mfma_f32_16x16x32_bf16 v[56:59], v[224:227], v[196:199], v[56:59]
	v_pk_max_i16 v11, v11, 0
	ds_read_b128 v[224:227], v121 offset:24576
	ds_read_b128 v[228:231], v121 offset:25600
	s_waitcnt lgkmcnt(6)
	v_mfma_f32_16x16x32_bf16 v[64:67], v[232:235], v[200:203], v[64:67]
	v_mfma_f32_16x16x32_bf16 v[68:71], v[236:239], v[200:203], v[68:71]
	s_mov_b32 m0, s28
	s_add_i32 s51, s50, 0x28000
	v_mfma_f32_16x16x32_bf16 v[60:63], v[236:239], v[204:207], v[60:63]
	buffer_load_dwordx4 v125, s[36:39], s51 offen lds
	v_mfma_f32_16x16x32_bf16 v[56:59], v[232:235], v[204:207], v[56:59]
	ds_read_b128 v[232:235], v121 offset:26624
	ds_read_b128 v[236:239], v121 offset:27648
	s_waitcnt lgkmcnt(6)
	ds_read_b128 v[152:155], v183 offset:1536
	ds_read_b128 v[156:159], v183 offset:1600
	v_mfma_f32_16x16x32_bf16 v[64:67], v[240:243], v[208:211], v[64:67]
	v_mfma_f32_16x16x32_bf16 v[68:71], v[244:247], v[208:211], v[68:71]
	s_mov_b32 m0, s29
	s_add_i32 s51, s50, 0x2a000
	v_mfma_f32_16x16x32_bf16 v[60:63], v[244:247], v[212:215], v[60:63]
	buffer_load_dwordx4 v125, s[36:39], s51 offen lds
	v_mfma_f32_16x16x32_bf16 v[56:59], v[240:243], v[212:215], v[56:59]
	ds_read_b128 v[240:243], v121 offset:28672
	ds_read_b128 v[244:247], v121 offset:29696
	s_waitcnt lgkmcnt(8)
	v_mfma_f32_16x16x32_bf16 v[64:67], v[248:251], v[216:219], v[64:67]
	v_mfma_f32_16x16x32_bf16 v[68:71], v[252:255], v[216:219], v[68:71]
	s_mov_b32 m0, s33
	s_add_i32 s51, s50, 0x2c000
	v_mfma_f32_16x16x32_bf16 v[60:63], v[252:255], v[220:223], v[60:63]
	buffer_load_dwordx4 v125, s[36:39], s51 offen lds
	v_mfma_f32_16x16x32_bf16 v[56:59], v[248:251], v[220:223], v[56:59]
	ds_read_b128 v[248:251], v121 offset:30720
	ds_read_b128 v[252:255], v121 offset:31744
	s_setprio 1
	s_waitcnt lgkmcnt(8)
	v_mfma_f32_16x16x32_bf16 v[80:83], v[224:227], v[88:91], v[160:163]
	v_mfma_f32_16x16x32_bf16 v[76:79], v[228:231], v[88:91], v[164:167]
	s_mov_b32 m0, s34
	s_add_i32 s51, s50, 0x2e000
	v_mfma_f32_16x16x32_bf16 v[72:75], v[228:231], v[92:95], v[164:167]
	buffer_load_dwordx4 v125, s[36:39], s51 offen lds
	v_mfma_f32_16x16x32_bf16 v[84:87], v[224:227], v[92:95], v[160:163]
	ds_read_b128 v[224:227], v121 offset:32768
	ds_read_b128 v[228:231], v121 offset:33792
	s_waitcnt lgkmcnt(8)
	v_mfma_f32_16x16x32_bf16 v[80:83], v[232:235], v[96:99], v[80:83]
	v_mfma_f32_16x16x32_bf16 v[76:79], v[236:239], v[96:99], v[76:79]
	v_mfma_f32_16x16x32_bf16 v[72:75], v[236:239], v[100:103], v[72:75]
	v_mfma_f32_16x16x32_bf16 v[84:87], v[232:235], v[100:103], v[84:87]
	ds_read_b128 v[232:235], v121 offset:34816
	ds_read_b128 v[236:239], v121 offset:35840
	s_waitcnt lgkmcnt(6)
	v_mfma_f32_16x16x32_bf16 v[80:83], v[240:243], v[104:107], v[80:83]
	v_cvt_pk_bf16_f32 v16, v64, v65
	v_mfma_f32_16x16x32_bf16 v[76:79], v[244:247], v[104:107], v[76:79]
	v_cvt_pk_bf16_f32 v17, v66, v67
	v_mfma_f32_16x16x32_bf16 v[72:75], v[244:247], v[108:111], v[72:75]
	v_cvt_pk_bf16_f32 v18, v68, v69
	v_mfma_f32_16x16x32_bf16 v[84:87], v[240:243], v[108:111], v[84:87]
	v_cvt_pk_bf16_f32 v19, v70, v71
	ds_read_b128 v[240:243], v121 offset:36864
	ds_read_b128 v[244:247], v121 offset:37888
	s_waitcnt lgkmcnt(6)
	v_mfma_f32_16x16x32_bf16 v[80:83], v[248:251], v[184:187], v[80:83]
	v_cvt_pk_bf16_f32 v20, v56, v57
	v_mfma_f32_16x16x32_bf16 v[76:79], v[252:255], v[184:187], v[76:79]
	v_cvt_pk_bf16_f32 v21, v58, v59
	v_mfma_f32_16x16x32_bf16 v[72:75], v[252:255], v[188:191], v[72:75]
	v_cvt_pk_bf16_f32 v22, v60, v61
	v_mfma_f32_16x16x32_bf16 v[84:87], v[248:251], v[188:191], v[84:87]
	v_cvt_pk_bf16_f32 v23, v62, v63
	ds_read_b128 v[248:251], v121 offset:38912
	ds_read_b128 v[252:255], v121 offset:39936
	s_setprio 0
	s_waitcnt lgkmcnt(6)
	v_mfma_f32_16x16x32_bf16 v[80:83], v[224:227], v[192:195], v[80:83]
	v_pk_max_i16 v16, v16, 0
	v_mfma_f32_16x16x32_bf16 v[76:79], v[228:231], v[192:195], v[76:79]
	v_pk_max_i16 v17, v17, 0
	v_mfma_f32_16x16x32_bf16 v[72:75], v[228:231], v[196:199], v[72:75]
	v_pk_max_i16 v18, v18, 0
	v_mfma_f32_16x16x32_bf16 v[84:87], v[224:227], v[196:199], v[84:87]
	v_pk_max_i16 v19, v19, 0
	s_waitcnt lgkmcnt(4)
	v_mfma_f32_16x16x32_bf16 v[80:83], v[232:235], v[200:203], v[80:83]
	v_pk_max_i16 v20, v20, 0
	v_mfma_f32_16x16x32_bf16 v[76:79], v[236:239], v[200:203], v[76:79]
	v_pk_max_i16 v21, v21, 0
	v_mfma_f32_16x16x32_bf16 v[72:75], v[236:239], v[204:207], v[72:75]
	v_pk_max_i16 v22, v22, 0
	v_mfma_f32_16x16x32_bf16 v[84:87], v[232:235], v[204:207], v[84:87]
	v_pk_max_i16 v23, v23, 0
.Lnerf_hid_b6:
	s_waitcnt vmcnt(0) lgkmcnt(0)
	s_barrier
	ds_read_b128 v[224:227], v121 offset:40960
	ds_read_b128 v[228:231], v121 offset:41984
	v_mfma_f32_16x16x32_bf16 v[80:83], v[240:243], v[208:211], v[80:83]
	ds_read_b128 v[232:235], v121 offset:43008
	v_mfma_f32_16x16x32_bf16 v[76:79], v[244:247], v[208:211], v[76:79]
	ds_read_b128 v[236:239], v121 offset:44032
	v_mfma_f32_16x16x32_bf16 v[72:75], v[244:247], v[212:215], v[72:75]
	v_mfma_f32_16x16x32_bf16 v[84:87], v[240:243], v[212:215], v[84:87]
	ds_read_b128 v[240:243], v121 offset:45056
	ds_read_b128 v[244:247], v121 offset:46080
	v_mfma_f32_16x16x32_bf16 v[80:83], v[248:251], v[216:219], v[80:83]
	v_mfma_f32_16x16x32_bf16 v[76:79], v[252:255], v[216:219], v[76:79]
	v_mfma_f32_16x16x32_bf16 v[72:75], v[252:255], v[220:223], v[72:75]
	v_mfma_f32_16x16x32_bf16 v[84:87], v[248:251], v[220:223], v[84:87]
	ds_read_b128 v[248:251], v121 offset:47104
	ds_read_b128 v[252:255], v121 offset:48128
	s_setprio 3
	s_waitcnt lgkmcnt(6)
	v_mfma_f32_16x16x32_bf16 v[64:67], v[224:227], v[88:91], v[152:155]
	v_mfma_f32_16x16x32_bf16 v[68:71], v[228:231], v[88:91], v[156:159]
	v_mfma_f32_16x16x32_bf16 v[60:63], v[228:231], v[92:95], v[156:159]
	v_mfma_f32_16x16x32_bf16 v[56:59], v[224:227], v[92:95], v[152:155]
	ds_read_b128 v[224:227], v121 offset:49152
	ds_read_b128 v[228:231], v121 offset:50176
	s_waitcnt lgkmcnt(6)
	ds_read_b128 v[160:163], v183 offset:1664
	ds_read_b128 v[164:167], v183 offset:1728
	v_mfma_f32_16x16x32_bf16 v[64:67], v[232:235], v[96:99], v[64:67]
	v_cvt_pk_bf16_f32 v24, v80, v81
	v_mfma_f32_16x16x32_bf16 v[68:71], v[236:239], v[96:99], v[68:71]
	v_cvt_pk_bf16_f32 v25, v82, v83
	v_mfma_f32_16x16x32_bf16 v[60:63], v[236:239], v[100:103], v[60:63]
	v_cvt_pk_bf16_f32 v26, v76, v77
	v_mfma_f32_16x16x32_bf16 v[56:59], v[232:235], v[100:103], v[56:59]
	v_cvt_pk_bf16_f32 v27, v78, v79
	ds_read_b128 v[232:235], v121 offset:51200
	ds_read_b128 v[236:239], v121 offset:52224
	s_waitcnt lgkmcnt(8)
	v_mfma_f32_16x16x32_bf16 v[64:67], v[240:243], v[104:107], v[64:67]
	v_cvt_pk_bf16_f32 v28, v84, v85
	v_mfma_f32_16x16x32_bf16 v[68:71], v[244:247], v[104:107], v[68:71]
	v_cvt_pk_bf16_f32 v29, v86, v87
	v_mfma_f32_16x16x32_bf16 v[60:63], v[244:247], v[108:111], v[60:63]
	v_cvt_pk_bf16_f32 v30, v72, v73
	v_mfma_f32_16x16x32_bf16 v[56:59], v[240:243], v[108:111], v[56:59]
	v_cvt_pk_bf16_f32 v31, v74, v75
	ds_read_b128 v[240:243], v121 offset:53248
	ds_read_b128 v[244:247], v121 offset:54272
	s_waitcnt lgkmcnt(8)
	v_mfma_f32_16x16x32_bf16 v[64:67], v[248:251], v[184:187], v[64:67]
	v_pk_max_i16 v24, v24, 0
	v_mfma_f32_16x16x32_bf16 v[68:71], v[252:255], v[184:187], v[68:71]
	v_pk_max_i16 v25, v25, 0
	v_mfma_f32_16x16x32_bf16 v[60:63], v[252:255], v[188:191], v[60:63]
	v_pk_max_i16 v26, v26, 0
	v_mfma_f32_16x16x32_bf16 v[56:59], v[248:251], v[188:191], v[56:59]
	v_pk_max_i16 v27, v27, 0
	ds_read_b128 v[248:251], v121 offset:55296
	ds_read_b128 v[252:255], v121 offset:56320
	s_setprio 2
	s_waitcnt lgkmcnt(8)
	v_mfma_f32_16x16x32_bf16 v[64:67], v[224:227], v[192:195], v[64:67]
	v_pk_max_i16 v28, v28, 0
	v_mfma_f32_16x16x32_bf16 v[68:71], v[228:231], v[192:195], v[68:71]
	v_pk_max_i16 v29, v29, 0
	v_mfma_f32_16x16x32_bf16 v[60:63], v[228:231], v[196:199], v[60:63]
	v_pk_max_i16 v30, v30, 0
	v_mfma_f32_16x16x32_bf16 v[56:59], v[224:227], v[196:199], v[56:59]
	v_pk_max_i16 v31, v31, 0
	ds_read_b128 v[224:227], v121 offset:57344
	ds_read_b128 v[228:231], v121 offset:58368
	s_waitcnt lgkmcnt(6)
	v_mfma_f32_16x16x32_bf16 v[64:67], v[232:235], v[200:203], v[64:67]
	v_mfma_f32_16x16x32_bf16 v[68:71], v[236:239], v[200:203], v[68:71]
	s_mov_b32 m0, s35
	s_add_i32 s51, s50, 0x30000
	v_mfma_f32_16x16x32_bf16 v[60:63], v[236:239], v[204:207], v[60:63]
	buffer_load_dwordx4 v125, s[36:39], s51 offen lds
	v_mfma_f32_16x16x32_bf16 v[56:59], v[232:235], v[204:207], v[56:59]
	ds_read_b128 v[232:235], v121 offset:59392
	ds_read_b128 v[236:239], v121 offset:60416
	s_waitcnt lgkmcnt(6)
	ds_read_b128 v[152:155], v183 offset:1792
	ds_read_b128 v[156:159], v183 offset:1856
	v_mfma_f32_16x16x32_bf16 v[64:67], v[240:243], v[208:211], v[64:67]
	v_mfma_f32_16x16x32_bf16 v[68:71], v[244:247], v[208:211], v[68:71]
	s_mov_b32 m0, s42
	s_add_i32 s51, s50, 0x32000
	v_mfma_f32_16x16x32_bf16 v[60:63], v[244:247], v[212:215], v[60:63]
	buffer_load_dwordx4 v125, s[36:39], s51 offen lds
	v_mfma_f32_16x16x32_bf16 v[56:59], v[240:243], v[212:215], v[56:59]
	ds_read_b128 v[240:243], v121 offset:61440
	ds_read_b128 v[244:247], v121 offset:62464
	s_waitcnt lgkmcnt(8)
	v_mfma_f32_16x16x32_bf16 v[64:67], v[248:251], v[216:219], v[64:67]
	v_mfma_f32_16x16x32_bf16 v[68:71], v[252:255], v[216:219], v[68:71]
	s_mov_b32 m0, s41
	s_add_i32 s51, s50, 0x34000
	v_mfma_f32_16x16x32_bf16 v[60:63], v[252:255], v[220:223], v[60:63]
	buffer_load_dwordx4 v125, s[36:39], s51 offen lds
	v_mfma_f32_16x16x32_bf16 v[56:59], v[248:251], v[220:223], v[56:59]
	ds_read_b128 v[248:251], v121 offset:63488
	ds_read_b128 v[252:255], v121 offset:64512
	s_setprio 1
	s_waitcnt lgkmcnt(8)
	v_mfma_f32_16x16x32_bf16 v[80:83], v[224:227], v[88:91], v[160:163]
	v_mfma_f32_16x16x32_bf16 v[76:79], v[228:231], v[88:91], v[164:167]
	s_mov_b32 m0, s40
	s_add_i32 s51, s50, 0x36000
	v_mfma_f32_16x16x32_bf16 v[72:75], v[228:231], v[92:95], v[164:167]
	buffer_load_dwordx4 v125, s[36:39], s51 offen lds
	v_mfma_f32_16x16x32_bf16 v[84:87], v[224:227], v[92:95], v[160:163]
	ds_read_b128 v[224:227], v126 offset:57344
	ds_read_b128 v[228:231], v126 offset:58368
	s_waitcnt lgkmcnt(8)
	v_mfma_f32_16x16x32_bf16 v[80:83], v[232:235], v[96:99], v[80:83]
	v_mfma_f32_16x16x32_bf16 v[76:79], v[236:239], v[96:99], v[76:79]
	v_mfma_f32_16x16x32_bf16 v[72:75], v[236:239], v[100:103], v[72:75]
	v_mfma_f32_16x16x32_bf16 v[84:87], v[232:235], v[100:103], v[84:87]
	ds_read_b128 v[232:235], v126 offset:59392
	ds_read_b128 v[236:239], v126 offset:60416
	s_waitcnt lgkmcnt(6)
	v_mfma_f32_16x16x32_bf16 v[80:83], v[240:243], v[104:107], v[80:83]
	v_cvt_pk_bf16_f32 v32, v64, v65
	v_mfma_f32_16x16x32_bf16 v[76:79], v[244:247], v[104:107], v[76:79]
	v_cvt_pk_bf16_f32 v33, v66, v67
	v_mfma_f32_16x16x32_bf16 v[72:75], v[244:247], v[108:111], v[72:75]
	v_cvt_pk_bf16_f32 v34, v68, v69
	v_mfma_f32_16x16x32_bf16 v[84:87], v[240:243], v[108:111], v[84:87]
	v_cvt_pk_bf16_f32 v35, v70, v71
	ds_read_b128 v[240:243], v126 offset:61440
	ds_read_b128 v[244:247], v126 offset:62464
	s_waitcnt lgkmcnt(6)
	v_mfma_f32_16x16x32_bf16 v[80:83], v[248:251], v[184:187], v[80:83]
	v_cvt_pk_bf16_f32 v36, v56, v57
	v_mfma_f32_16x16x32_bf16 v[76:79], v[252:255], v[184:187], v[76:79]
	v_cvt_pk_bf16_f32 v37, v58, v59
	v_mfma_f32_16x16x32_bf16 v[72:75], v[252:255], v[188:191], v[72:75]
	v_cvt_pk_bf16_f32 v38, v60, v61
	v_mfma_f32_16x16x32_bf16 v[84:87], v[248:251], v[188:191], v[84:87]
	v_cvt_pk_bf16_f32 v39, v62, v63
	ds_read_b128 v[248:251], v126 offset:63488
	ds_read_b128 v[252:255], v126 offset:64512
	s_setprio 0
	s_waitcnt lgkmcnt(6)
	v_mfma_f32_16x16x32_bf16 v[80:83], v[224:227], v[192:195], v[80:83]
	v_pk_max_i16 v32, v32, 0
	v_mfma_f32_16x16x32_bf16 v[76:79], v[228:231], v[192:195], v[76:79]
	v_pk_max_i16 v33, v33, 0
	v_mfma_f32_16x16x32_bf16 v[72:75], v[228:231], v[196:199], v[72:75]
	v_pk_max_i16 v34, v34, 0
	v_mfma_f32_16x16x32_bf16 v[84:87], v[224:227], v[196:199], v[84:87]
	v_pk_max_i16 v35, v35, 0
	s_waitcnt lgkmcnt(4)
	v_mfma_f32_16x16x32_bf16 v[80:83], v[232:235], v[200:203], v[80:83]
	v_pk_max_i16 v36, v36, 0
	v_mfma_f32_16x16x32_bf16 v[76:79], v[236:239], v[200:203], v[76:79]
	v_pk_max_i16 v37, v37, 0
	v_mfma_f32_16x16x32_bf16 v[72:75], v[236:239], v[204:207], v[72:75]
	v_pk_max_i16 v38, v38, 0
	v_mfma_f32_16x16x32_bf16 v[84:87], v[232:235], v[204:207], v[84:87]
	v_pk_max_i16 v39, v39, 0
.Lnerf_hid_b7:
	s_waitcnt vmcnt(0) lgkmcnt(0)
	s_barrier
	ds_read_b128 v[224:227], v121 offset:8192
	ds_read_b128 v[228:231], v121 offset:9216
	v_mfma_f32_16x16x32_bf16 v[80:83], v[240:243], v[208:211], v[80:83]
	ds_read_b128 v[232:235], v121 offset:10240
	v_mfma_f32_16x16x32_bf16 v[76:79], v[244:247], v[208:211], v[76:79]
	ds_read_b128 v[236:239], v121 offset:11264
	v_mfma_f32_16x16x32_bf16 v[72:75], v[244:247], v[212:215], v[72:75]
	v_mfma_f32_16x16x32_bf16 v[84:87], v[240:243], v[212:215], v[84:87]
	ds_read_b128 v[240:243], v121 offset:12288
	ds_read_b128 v[244:247], v121 offset:13312
	v_mfma_f32_16x16x32_bf16 v[80:83], v[248:251], v[216:219], v[80:83]
	v_mfma_f32_16x16x32_bf16 v[76:79], v[252:255], v[216:219], v[76:79]
	v_mfma_f32_16x16x32_bf16 v[72:75], v[252:255], v[220:223], v[72:75]
	v_mfma_f32_16x16x32_bf16 v[84:87], v[248:251], v[220:223], v[84:87]
	ds_read_b128 v[248:251], v121 offset:14336
	ds_read_b128 v[252:255], v121 offset:15360
	s_setprio 3
	s_waitcnt lgkmcnt(6)
	v_mfma_f32_16x16x32_bf16 v[64:67], v[224:227], v[88:91], v[152:155]
	v_mfma_f32_16x16x32_bf16 v[68:71], v[228:231], v[88:91], v[156:159]
	v_mfma_f32_16x16x32_bf16 v[60:63], v[228:231], v[92:95], v[156:159]
	v_mfma_f32_16x16x32_bf16 v[56:59], v[224:227], v[92:95], v[152:155]
	ds_read_b128 v[224:227], v121 offset:16384
	ds_read_b128 v[228:231], v121 offset:17408
	s_waitcnt lgkmcnt(6)
	ds_read_b128 v[160:163], v183 offset:1920
	ds_read_b128 v[164:167], v183 offset:1984
	v_mfma_f32_16x16x32_bf16 v[64:67], v[232:235], v[96:99], v[64:67]
	v_cvt_pk_bf16_f32 v40, v80, v81
	v_mfma_f32_16x16x32_bf16 v[68:71], v[236:239], v[96:99], v[68:71]
	v_cvt_pk_bf16_f32 v41, v82, v83
	v_mfma_f32_16x16x32_bf16 v[60:63], v[236:239], v[100:103], v[60:63]
	v_cvt_pk_bf16_f32 v42, v76, v77
	v_mfma_f32_16x16x32_bf16 v[56:59], v[232:235], v[100:103], v[56:59]
	v_cvt_pk_bf16_f32 v43, v78, v79
	ds_read_b128 v[232:235], v121 offset:18432
	ds_read_b128 v[236:239], v121 offset:19456
	s_waitcnt lgkmcnt(8)
	v_mfma_f32_16x16x32_bf16 v[64:67], v[240:243], v[104:107], v[64:67]
	v_cvt_pk_bf16_f32 v44, v84, v85
	v_mfma_f32_16x16x32_bf16 v[68:71], v[244:247], v[104:107], v[68:71]
	v_cvt_pk_bf16_f32 v45, v86, v87
	v_mfma_f32_16x16x32_bf16 v[60:63], v[244:247], v[108:111], v[60:63]
	v_cvt_pk_bf16_f32 v46, v72, v73
	v_mfma_f32_16x16x32_bf16 v[56:59], v[240:243], v[108:111], v[56:59]
	v_cvt_pk_bf16_f32 v47, v74, v75
	ds_read_b128 v[240:243], v121 offset:20480
	ds_read_b128 v[244:247], v121 offset:21504
	s_waitcnt lgkmcnt(8)
	v_mfma_f32_16x16x32_bf16 v[64:67], v[248:251], v[184:187], v[64:67]
	v_pk_max_i16 v40, v40, 0
	v_mfma_f32_16x16x32_bf16 v[68:71], v[252:255], v[184:187], v[68:71]
	v_pk_max_i16 v41, v41, 0
	v_mfma_f32_16x16x32_bf16 v[60:63], v[252:255], v[188:191], v[60:63]
	v_pk_max_i16 v42, v42, 0
	v_mfma_f32_16x16x32_bf16 v[56:59], v[248:251], v[188:191], v[56:59]
	v_pk_max_i16 v43, v43, 0
	ds_read_b128 v[248:251], v121 offset:22528
	ds_read_b128 v[252:255], v121 offset:23552
	s_setprio 2
	s_waitcnt lgkmcnt(8)
	v_mfma_f32_16x16x32_bf16 v[64:67], v[224:227], v[192:195], v[64:67]
	v_pk_max_i16 v44, v44, 0
	v_mfma_f32_16x16x32_bf16 v[68:71], v[228:231], v[192:195], v[68:71]
	v_pk_max_i16 v45, v45, 0
	v_mfma_f32_16x16x32_bf16 v[60:63], v[228:231], v[196:199], v[60:63]
	v_pk_max_i16 v46, v46, 0
	v_mfma_f32_16x16x32_bf16 v[56:59], v[224:227], v[196:199], v[56:59]
	v_pk_max_i16 v47, v47, 0
	ds_read_b128 v[224:227], v121 offset:24576
	ds_read_b128 v[228:231], v121 offset:25600
	s_waitcnt lgkmcnt(6)
	v_mfma_f32_16x16x32_bf16 v[64:67], v[232:235], v[200:203], v[64:67]
	v_mfma_f32_16x16x32_bf16 v[68:71], v[236:239], v[200:203], v[68:71]
	s_mov_b32 m0, s28
	s_add_i32 s51, s50, 0x38000
	v_mfma_f32_16x16x32_bf16 v[60:63], v[236:239], v[204:207], v[60:63]
	buffer_load_dwordx4 v125, s[36:39], s51 offen lds
	v_mfma_f32_16x16x32_bf16 v[56:59], v[232:235], v[204:207], v[56:59]
	ds_read_b128 v[232:235], v121 offset:26624
	ds_read_b128 v[236:239], v121 offset:27648
	s_waitcnt lgkmcnt(6)
	ds_read_b128 v[152:155], v183 offset:2048
	ds_read_b128 v[156:159], v183 offset:2112
	v_mfma_f32_16x16x32_bf16 v[64:67], v[240:243], v[208:211], v[64:67]
	v_mfma_f32_16x16x32_bf16 v[68:71], v[244:247], v[208:211], v[68:71]
	s_mov_b32 m0, s29
	s_add_i32 s51, s50, 0x3a000
	v_mfma_f32_16x16x32_bf16 v[60:63], v[244:247], v[212:215], v[60:63]
	buffer_load_dwordx4 v125, s[36:39], s51 offen lds
	v_mfma_f32_16x16x32_bf16 v[56:59], v[240:243], v[212:215], v[56:59]
	ds_read_b128 v[240:243], v121 offset:28672
	ds_read_b128 v[244:247], v121 offset:29696
	s_waitcnt lgkmcnt(8)
	v_mfma_f32_16x16x32_bf16 v[64:67], v[248:251], v[216:219], v[64:67]
	v_mfma_f32_16x16x32_bf16 v[68:71], v[252:255], v[216:219], v[68:71]
	s_mov_b32 m0, s33
	s_add_i32 s51, s50, 0x3c000
	v_mfma_f32_16x16x32_bf16 v[60:63], v[252:255], v[220:223], v[60:63]
	buffer_load_dwordx4 v125, s[36:39], s51 offen lds
	v_mfma_f32_16x16x32_bf16 v[56:59], v[248:251], v[220:223], v[56:59]
	ds_read_b128 v[248:251], v121 offset:30720
	ds_read_b128 v[252:255], v121 offset:31744
	s_setprio 1
	s_waitcnt lgkmcnt(8)
	v_mfma_f32_16x16x32_bf16 v[80:83], v[224:227], v[88:91], v[160:163]
	v_mfma_f32_16x16x32_bf16 v[76:79], v[228:231], v[88:91], v[164:167]
	s_mov_b32 m0, s34
	s_add_i32 s51, s50, 0x3e000
	v_mfma_f32_16x16x32_bf16 v[72:75], v[228:231], v[92:95], v[164:167]
	buffer_load_dwordx4 v125, s[36:39], s51 offen lds
	v_mfma_f32_16x16x32_bf16 v[84:87], v[224:227], v[92:95], v[160:163]
	ds_read_b128 v[224:227], v121 offset:32768
	ds_read_b128 v[228:231], v121 offset:33792
	s_waitcnt lgkmcnt(8)
	v_mfma_f32_16x16x32_bf16 v[80:83], v[232:235], v[96:99], v[80:83]
	v_mfma_f32_16x16x32_bf16 v[76:79], v[236:239], v[96:99], v[76:79]
	v_mfma_f32_16x16x32_bf16 v[72:75], v[236:239], v[100:103], v[72:75]
	v_mfma_f32_16x16x32_bf16 v[84:87], v[232:235], v[100:103], v[84:87]
	ds_read_b128 v[232:235], v121 offset:34816
	ds_read_b128 v[236:239], v121 offset:35840
	s_waitcnt lgkmcnt(6)
	v_mfma_f32_16x16x32_bf16 v[80:83], v[240:243], v[104:107], v[80:83]
	v_cvt_pk_bf16_f32 v48, v64, v65
	v_mfma_f32_16x16x32_bf16 v[76:79], v[244:247], v[104:107], v[76:79]
	v_cvt_pk_bf16_f32 v49, v66, v67
	v_mfma_f32_16x16x32_bf16 v[72:75], v[244:247], v[108:111], v[72:75]
	v_cvt_pk_bf16_f32 v50, v68, v69
	v_mfma_f32_16x16x32_bf16 v[84:87], v[240:243], v[108:111], v[84:87]
	v_cvt_pk_bf16_f32 v51, v70, v71
	ds_read_b128 v[240:243], v121 offset:36864
	ds_read_b128 v[244:247], v121 offset:37888
	s_waitcnt lgkmcnt(6)
	v_mfma_f32_16x16x32_bf16 v[80:83], v[248:251], v[184:187], v[80:83]
	v_cvt_pk_bf16_f32 v52, v56, v57
	v_mfma_f32_16x16x32_bf16 v[76:79], v[252:255], v[184:187], v[76:79]
	v_cvt_pk_bf16_f32 v53, v58, v59
	v_mfma_f32_16x16x32_bf16 v[72:75], v[252:255], v[188:191], v[72:75]
	v_cvt_pk_bf16_f32 v54, v60, v61
	v_mfma_f32_16x16x32_bf16 v[84:87], v[248:251], v[188:191], v[84:87]
	v_cvt_pk_bf16_f32 v55, v62, v63
	ds_read_b128 v[248:251], v121 offset:38912
	ds_read_b128 v[252:255], v121 offset:39936
	s_setprio 0
	s_waitcnt lgkmcnt(6)
	v_mfma_f32_16x16x32_bf16 v[80:83], v[224:227], v[192:195], v[80:83]
	v_pk_max_i16 v48, v48, 0
	v_mfma_f32_16x16x32_bf16 v[76:79], v[228:231], v[192:195], v[76:79]
	v_pk_max_i16 v49, v49, 0
	v_mfma_f32_16x16x32_bf16 v[72:75], v[228:231], v[196:199], v[72:75]
	v_pk_max_i16 v50, v50, 0
	v_mfma_f32_16x16x32_bf16 v[84:87], v[224:227], v[196:199], v[84:87]
	v_pk_max_i16 v51, v51, 0
	s_waitcnt lgkmcnt(4)
	v_mfma_f32_16x16x32_bf16 v[80:83], v[232:235], v[200:203], v[80:83]
	v_pk_max_i16 v52, v52, 0
	v_mfma_f32_16x16x32_bf16 v[76:79], v[236:239], v[200:203], v[76:79]
	v_pk_max_i16 v53, v53, 0
	v_mfma_f32_16x16x32_bf16 v[72:75], v[236:239], v[204:207], v[72:75]
	v_pk_max_i16 v54, v54, 0
	v_mfma_f32_16x16x32_bf16 v[84:87], v[232:235], v[204:207], v[84:87]
	v_pk_max_i16 v55, v55, 0
	s_add_i32 s50, s50, 0x40000
	v_add_u32_e32 v183, 0x800, v183
	s_add_i32 s52, s52, 1
	s_branch .Lnerf_hid_b0
